# K1 prologue rewritten: all 16 x loads + 20 codebook loads issued up-front, x bf16 split overlapped with codebook latency
# speedup vs baseline: 1.0499x; 1.0271x over previous
.LBB0_4:
	s_load_dwordx2 s[12:13], s[0:1], 0x10
	s_load_dwordx4 s[20:23], s[0:1], 0x0
	v_lshrrev_b32_e32 v1, 6, v0
	v_and_b32_e32 v130, 15, v0
	v_cmp_le_u32_e32 vcc, s4, v1
	s_and_saveexec_b64 s[4:5], vcc
	s_xor_b64 s[4:5], exec, s[4:5]
	s_cbranch_execz .LBB0_6
	v_lshlrev_b32_e32 v2, 2, v130
	v_lshl_or_b32 v2, v1, 10, v2
	v_or_b32_e32 v3, 0x20000, v2
	v_mov_b32_e32 v4, 0
	ds_write_b32 v3, v4
	v_or_b32_e32 v3, 0x20200, v2
	ds_write_b32 v3, v4
	v_or_b32_e32 v3, 0x20040, v2
	ds_write_b32 v3, v4
	v_or_b32_e32 v3, 0x20240, v2
	ds_write_b32 v3, v4
	v_or_b32_e32 v3, 0x20080, v2
	ds_write_b32 v3, v4
	v_or_b32_e32 v3, 0x20280, v2
	ds_write_b32 v3, v4
	v_or_b32_e32 v3, 0x200c0, v2
	ds_write_b32 v3, v4
	v_or_b32_e32 v3, 0x202c0, v2
	ds_write_b32 v3, v4
	v_or_b32_e32 v3, 0x20100, v2
	ds_write_b32 v3, v4
	v_or_b32_e32 v3, 0x20300, v2
	ds_write_b32 v3, v4
	v_or_b32_e32 v3, 0x20140, v2
	ds_write_b32 v3, v4
	v_or_b32_e32 v3, 0x20340, v2
	ds_write_b32 v3, v4
	v_or_b32_e32 v3, 0x20180, v2
	ds_write_b32 v3, v4
	v_or_b32_e32 v3, 0x20380, v2
	ds_write_b32 v3, v4
	v_or_b32_e32 v3, 0x201c0, v2
	v_or_b32_e32 v2, 0x203c0, v2
	ds_write_b32 v3, v4
	ds_write_b32 v2, v4
.LBB0_6:
	s_or_saveexec_b64 s[14:15], s[4:5]
	v_and_b32_e32 v194, 63, v0
	s_bfe_u32 s17, s2, 0x30003
	v_mov_b32_e32 v195, 0
	v_mov_b32_e32 v58, 0
	v_mov_b32_e32 v59, 0
	v_mov_b32_e32 v60, 0
	v_mov_b32_e32 v61, 0
	v_mov_b32_e32 v62, 0
	v_mov_b32_e32 v63, 0
	v_mov_b32_e32 v64, 0
	v_mov_b32_e32 v65, 0
	v_mov_b32_e32 v74, 0
	v_mov_b32_e32 v75, 0
	v_mov_b32_e32 v76, 0
	v_mov_b32_e32 v77, 0
	v_mov_b32_e32 v78, 0
	v_mov_b32_e32 v79, 0
	v_mov_b32_e32 v80, 0
	v_mov_b32_e32 v81, 0
	v_mov_b32_e32 v82, 0
	v_mov_b32_e32 v83, 0
	v_mov_b32_e32 v84, 0
	v_mov_b32_e32 v85, 0
	v_mov_b32_e32 v86, 0
	v_mov_b32_e32 v87, 0
	v_mov_b32_e32 v88, 0
	v_mov_b32_e32 v89, 0
	v_mov_b32_e32 v90, 0
	v_mov_b32_e32 v91, 0
	v_mov_b32_e32 v92, 0
	v_mov_b32_e32 v93, 0
	v_mov_b32_e32 v94, 0
	v_mov_b32_e32 v95, 0
	v_mov_b32_e32 v96, 0
	v_mov_b32_e32 v97, 0
	v_mov_b32_e32 v98, 0
	v_mov_b32_e32 v99, 0
	v_mov_b32_e32 v100, 0
	v_mov_b32_e32 v101, 0
	v_mov_b32_e32 v102, 0
	v_mov_b32_e32 v103, 0
	v_mov_b32_e32 v104, 0
	v_mov_b32_e32 v105, 0
	v_mov_b32_e32 v106, 0
	v_mov_b32_e32 v107, 0
	v_mov_b32_e32 v108, 0
	v_mov_b32_e32 v109, 0
	v_mov_b32_e32 v110, 0
	v_mov_b32_e32 v111, 0
	v_mov_b32_e32 v112, 0
	v_mov_b32_e32 v113, 0
	v_mov_b32_e32 v114, 0
	v_mov_b32_e32 v115, 0
	v_mov_b32_e32 v116, 0
	v_mov_b32_e32 v117, 0
	v_mov_b32_e32 v118, 0
	v_mov_b32_e32 v119, 0
	v_mov_b32_e32 v120, 0
	v_mov_b32_e32 v121, 0
	v_mov_b32_e32 v2, 0
	v_mov_b32_e32 v3, 0
	v_mov_b32_e32 v4, 0
	v_mov_b32_e32 v5, 0
	v_mov_b32_e32 v6, 0
	v_mov_b32_e32 v7, 0
	v_mov_b32_e32 v8, 0
	v_mov_b32_e32 v9, 0
	s_xor_b64 exec, exec, s[14:15]
	s_cbranch_execz .LBB0_8
	v_add_lshl_u32 v36, s3, v1, 7
	v_mul_u32_u24_e32 v82, 0x1f400, v130
	v_mov_b32_e32 v83, 0
	v_ashrrev_i32_e32 v37, 31, v36
	s_waitcnt lgkmcnt(0)
	v_lshl_add_u64 v[2:3], s[20:21], 0, v[82:83]
	v_lshl_add_u64 v[2:3], v[36:37], 2, v[2:3]
	v_and_b32_e32 v82, 48, v194
	v_lshl_add_u64 v[2:3], v[2:3], 0, v[82:83]
	s_mov_b32 s2, 0x1f4000
	v_add_co_u32_e32 v240, vcc, s2, v2
	v_lshrrev_b32_e32 v83, 4, v194
	s_nop 0
	v_addc_co_u32_e32 v241, vcc, 0, v3, vcc
	global_load_dwordx4 v[166:169], v[2:3], off
	global_load_dwordx4 v[170:173], v[2:3], off offset:64
	global_load_dwordx4 v[174:177], v[2:3], off offset:128
	global_load_dwordx4 v[178:181], v[2:3], off offset:192
	global_load_dwordx4 v[182:185], v[2:3], off offset:256
	global_load_dwordx4 v[186:189], v[2:3], off offset:320
	global_load_dwordx4 v[190:193], v[2:3], off offset:384
	global_load_dwordx4 v[204:207], v[2:3], off offset:448
	global_load_dwordx4 v[208:211], v[240:241], off
	global_load_dwordx4 v[212:215], v[240:241], off offset:64
	global_load_dwordx4 v[216:219], v[240:241], off offset:128
	global_load_dwordx4 v[220:223], v[240:241], off offset:192
	global_load_dwordx4 v[224:227], v[240:241], off offset:256
	global_load_dwordx4 v[228:231], v[240:241], off offset:320
	global_load_dwordx4 v[232:235], v[240:241], off offset:384
	global_load_dwordx4 v[236:239], v[240:241], off offset:448
	v_lshl_or_b32 v37, s17, 7, v83
	s_movk_i32 s3, 0x7d00
	v_mad_u32_u24 v36, v37, s3, v36
	v_lshlrev_b32_e32 v96, 4, v130
	s_and_b32 s9, s23, 0xffff
	s_mov_b32 s11, 0x20000
	s_mov_b32 s10, 0x7d00000
	s_mov_b32 s8, s22
	v_lshl_or_b32 v201, v36, 2, v96
	s_mov_b32 s3, 0x7d000
	buffer_load_dwordx4 v[122:125], v201, s[8:11], s3 offen nt
	s_mov_b32 s4, 0xfa000
	buffer_load_dwordx4 v[126:129], v201, s[8:11], s4 offen nt
	s_mov_b32 s3, 0x177000
	buffer_load_dwordx4 v[132:135], v201, s[8:11], s3 offen nt
	s_mov_b32 s4, 0x100
	buffer_load_dwordx4 v[136:139], v201, s[8:11], s4 offen nt
	s_mov_b32 s3, 0x7d100
	buffer_load_dwordx4 v[140:143], v201, s[8:11], s3 offen nt
	s_mov_b32 s4, 0xfa100
	buffer_load_dwordx4 v[154:157], v201, s[8:11], s4 offen nt
	buffer_load_dwordx4 v[158:161], v201, s[8:11], 0 offen nt
	s_mov_b32 s4, 0x1f4000
	buffer_load_dwordx4 v[58:61], v201, s[8:11], s4 offen nt
	s_mov_b32 s3, 0x177100
	buffer_load_dwordx4 v[162:165], v201, s[8:11], s3 offen nt
	s_mov_b32 s4, 0x271000
	buffer_load_dwordx4 v[62:65], v201, s[8:11], s4 offen nt
	s_mov_b32 s3, 0x2ee000
	buffer_load_dwordx4 v[98:101], v201, s[8:11], s3 offen nt
	s_mov_b32 s4, 0x36b000
	buffer_load_dwordx4 v[102:105], v201, s[8:11], s4 offen nt
	s_mov_b32 s3, 0x1f4100
	buffer_load_dwordx4 v[106:109], v201, s[8:11], s3 offen nt
	s_mov_b32 s4, 0x271100
	buffer_load_dwordx4 v[110:113], v201, s[8:11], s4 offen nt
	s_mov_b32 s3, 0x2ee100
	buffer_load_dwordx4 v[146:149], v201, s[8:11], s3 offen nt
	s_mov_b32 s4, 0x36b100
	buffer_load_dwordx4 v[150:153], v201, s[8:11], s4 offen nt
	s_mov_b32 s3, 0x3e8000
	buffer_load_dwordx4 v[74:77], v201, s[8:11], s3 offen nt
	s_mov_b32 s4, 0x465000
	buffer_load_dwordx4 v[78:81], v201, s[8:11], s4 offen nt
	s_mov_b32 s3, 0x4e2000
	buffer_load_dwordx4 v[114:117], v201, s[8:11], s3 offen nt
	s_mov_b32 s4, 0x55f000
	buffer_load_dwordx4 v[118:121], v201, s[8:11], s4 offen nt
	v_mul_u32_u24_e32 v86, 0x120, v130
	v_mul_u32_u24_e32 v84, 0x2400, v1
	v_mul_u32_u24_e32 v85, 0x120, v83
	v_add3_u32 v200, v84, v85, v96
	s_waitcnt vmcnt(34)
	v_cvt_pk_bf16_f32 v22, v166, v167
	v_cvt_pk_bf16_f32 v23, v168, v169
	v_cvt_pk_bf16_f32 v24, v170, v171
	v_cvt_pk_bf16_f32 v25, v172, v173
	v_lshlrev_b32_e32 v242, 16, v22
	v_and_b32_e32 v243, 0xffff0000, v22
	v_lshlrev_b32_e32 v244, 16, v23
	v_and_b32_e32 v245, 0xffff0000, v23
	v_lshlrev_b32_e32 v246, 16, v24
	v_and_b32_e32 v247, 0xffff0000, v24
	v_lshlrev_b32_e32 v248, 16, v25
	v_and_b32_e32 v249, 0xffff0000, v25
	v_pk_add_f32 v[242:243], v[166:167], v[242:243] neg_lo:[0,1] neg_hi:[0,1]
	v_pk_add_f32 v[244:245], v[168:169], v[244:245] neg_lo:[0,1] neg_hi:[0,1]
	v_pk_add_f32 v[246:247], v[170:171], v[246:247] neg_lo:[0,1] neg_hi:[0,1]
	v_pk_add_f32 v[248:249], v[172:173], v[248:249] neg_lo:[0,1] neg_hi:[0,1]
	v_cvt_pk_bf16_f32 v30, v242, v243
	v_cvt_pk_bf16_f32 v31, v244, v245
	v_cvt_pk_bf16_f32 v32, v246, v247
	v_cvt_pk_bf16_f32 v33, v248, v249
	s_waitcnt vmcnt(32)
	v_cvt_pk_bf16_f32 v18, v174, v175
	v_cvt_pk_bf16_f32 v19, v176, v177
	v_cvt_pk_bf16_f32 v20, v178, v179
	v_cvt_pk_bf16_f32 v21, v180, v181
	v_lshlrev_b32_e32 v242, 16, v18
	v_and_b32_e32 v243, 0xffff0000, v18
	v_lshlrev_b32_e32 v244, 16, v19
	v_and_b32_e32 v245, 0xffff0000, v19
	v_lshlrev_b32_e32 v246, 16, v20
	v_and_b32_e32 v247, 0xffff0000, v20
	v_lshlrev_b32_e32 v248, 16, v21
	v_and_b32_e32 v249, 0xffff0000, v21
	v_pk_add_f32 v[242:243], v[174:175], v[242:243] neg_lo:[0,1] neg_hi:[0,1]
	v_pk_add_f32 v[244:245], v[176:177], v[244:245] neg_lo:[0,1] neg_hi:[0,1]
	v_pk_add_f32 v[246:247], v[178:179], v[246:247] neg_lo:[0,1] neg_hi:[0,1]
	v_pk_add_f32 v[248:249], v[180:181], v[248:249] neg_lo:[0,1] neg_hi:[0,1]
	v_cvt_pk_bf16_f32 v26, v242, v243
	v_cvt_pk_bf16_f32 v27, v244, v245
	v_cvt_pk_bf16_f32 v28, v246, v247
	v_cvt_pk_bf16_f32 v29, v248, v249
	s_waitcnt vmcnt(30)
	v_cvt_pk_bf16_f32 v6, v182, v183
	v_cvt_pk_bf16_f32 v7, v184, v185
	v_cvt_pk_bf16_f32 v8, v186, v187
	v_cvt_pk_bf16_f32 v9, v188, v189
	v_lshlrev_b32_e32 v242, 16, v6
	v_and_b32_e32 v243, 0xffff0000, v6
	v_lshlrev_b32_e32 v244, 16, v7
	v_and_b32_e32 v245, 0xffff0000, v7
	v_lshlrev_b32_e32 v246, 16, v8
	v_and_b32_e32 v247, 0xffff0000, v8
	v_lshlrev_b32_e32 v248, 16, v9
	v_and_b32_e32 v249, 0xffff0000, v9
	v_pk_add_f32 v[242:243], v[182:183], v[242:243] neg_lo:[0,1] neg_hi:[0,1]
	v_pk_add_f32 v[244:245], v[184:185], v[244:245] neg_lo:[0,1] neg_hi:[0,1]
	v_pk_add_f32 v[246:247], v[186:187], v[246:247] neg_lo:[0,1] neg_hi:[0,1]
	v_pk_add_f32 v[248:249], v[188:189], v[248:249] neg_lo:[0,1] neg_hi:[0,1]
	v_cvt_pk_bf16_f32 v14, v242, v243
	v_cvt_pk_bf16_f32 v15, v244, v245
	v_cvt_pk_bf16_f32 v16, v246, v247
	v_cvt_pk_bf16_f32 v17, v248, v249
	s_waitcnt vmcnt(28)
	v_cvt_pk_bf16_f32 v2, v190, v191
	v_cvt_pk_bf16_f32 v3, v192, v193
	v_cvt_pk_bf16_f32 v4, v204, v205
	v_cvt_pk_bf16_f32 v5, v206, v207
	v_lshlrev_b32_e32 v242, 16, v2
	v_and_b32_e32 v243, 0xffff0000, v2
	v_lshlrev_b32_e32 v244, 16, v3
	v_and_b32_e32 v245, 0xffff0000, v3
	v_lshlrev_b32_e32 v246, 16, v4
	v_and_b32_e32 v247, 0xffff0000, v4
	v_lshlrev_b32_e32 v248, 16, v5
	v_and_b32_e32 v249, 0xffff0000, v5
	v_pk_add_f32 v[242:243], v[190:191], v[242:243] neg_lo:[0,1] neg_hi:[0,1]
	v_pk_add_f32 v[244:245], v[192:193], v[244:245] neg_lo:[0,1] neg_hi:[0,1]
	v_pk_add_f32 v[246:247], v[204:205], v[246:247] neg_lo:[0,1] neg_hi:[0,1]
	v_pk_add_f32 v[248:249], v[206:207], v[248:249] neg_lo:[0,1] neg_hi:[0,1]
	v_cvt_pk_bf16_f32 v10, v242, v243
	v_cvt_pk_bf16_f32 v11, v244, v245
	v_cvt_pk_bf16_f32 v12, v246, v247
	v_cvt_pk_bf16_f32 v13, v248, v249
	s_waitcnt vmcnt(26)
	v_cvt_pk_bf16_f32 v34, v208, v209
	v_cvt_pk_bf16_f32 v35, v210, v211
	v_cvt_pk_bf16_f32 v36, v212, v213
	v_cvt_pk_bf16_f32 v37, v214, v215
	v_lshlrev_b32_e32 v242, 16, v34
	v_and_b32_e32 v243, 0xffff0000, v34
	v_lshlrev_b32_e32 v244, 16, v35
	v_and_b32_e32 v245, 0xffff0000, v35
	v_lshlrev_b32_e32 v246, 16, v36
	v_and_b32_e32 v247, 0xffff0000, v36
	v_lshlrev_b32_e32 v248, 16, v37
	v_and_b32_e32 v249, 0xffff0000, v37
	v_pk_add_f32 v[242:243], v[208:209], v[242:243] neg_lo:[0,1] neg_hi:[0,1]
	v_pk_add_f32 v[244:245], v[210:211], v[244:245] neg_lo:[0,1] neg_hi:[0,1]
	v_pk_add_f32 v[246:247], v[212:213], v[246:247] neg_lo:[0,1] neg_hi:[0,1]
	v_pk_add_f32 v[248:249], v[214:215], v[248:249] neg_lo:[0,1] neg_hi:[0,1]
	v_cvt_pk_bf16_f32 v38, v242, v243
	v_cvt_pk_bf16_f32 v39, v244, v245
	v_cvt_pk_bf16_f32 v40, v246, v247
	v_cvt_pk_bf16_f32 v41, v248, v249
	s_waitcnt vmcnt(24)
	v_cvt_pk_bf16_f32 v66, v216, v217
	v_cvt_pk_bf16_f32 v67, v218, v219
	v_cvt_pk_bf16_f32 v68, v220, v221
	v_cvt_pk_bf16_f32 v69, v222, v223
	v_lshlrev_b32_e32 v242, 16, v66
	v_and_b32_e32 v243, 0xffff0000, v66
	v_lshlrev_b32_e32 v244, 16, v67
	v_and_b32_e32 v245, 0xffff0000, v67
	v_lshlrev_b32_e32 v246, 16, v68
	v_and_b32_e32 v247, 0xffff0000, v68
	v_lshlrev_b32_e32 v248, 16, v69
	v_and_b32_e32 v249, 0xffff0000, v69
	v_pk_add_f32 v[242:243], v[216:217], v[242:243] neg_lo:[0,1] neg_hi:[0,1]
	v_pk_add_f32 v[244:245], v[218:219], v[244:245] neg_lo:[0,1] neg_hi:[0,1]
	v_pk_add_f32 v[246:247], v[220:221], v[246:247] neg_lo:[0,1] neg_hi:[0,1]
	v_pk_add_f32 v[248:249], v[222:223], v[248:249] neg_lo:[0,1] neg_hi:[0,1]
	v_cvt_pk_bf16_f32 v70, v242, v243
	v_cvt_pk_bf16_f32 v71, v244, v245
	v_cvt_pk_bf16_f32 v72, v246, v247
	v_cvt_pk_bf16_f32 v73, v248, v249
	s_waitcnt vmcnt(22)
	v_cvt_pk_bf16_f32 v50, v224, v225
	v_cvt_pk_bf16_f32 v51, v226, v227
	v_cvt_pk_bf16_f32 v52, v228, v229
	v_cvt_pk_bf16_f32 v53, v230, v231
	v_lshlrev_b32_e32 v242, 16, v50
	v_and_b32_e32 v243, 0xffff0000, v50
	v_lshlrev_b32_e32 v244, 16, v51
	v_and_b32_e32 v245, 0xffff0000, v51
	v_lshlrev_b32_e32 v246, 16, v52
	v_and_b32_e32 v247, 0xffff0000, v52
	v_lshlrev_b32_e32 v248, 16, v53
	v_and_b32_e32 v249, 0xffff0000, v53
	v_pk_add_f32 v[242:243], v[224:225], v[242:243] neg_lo:[0,1] neg_hi:[0,1]
	v_pk_add_f32 v[244:245], v[226:227], v[244:245] neg_lo:[0,1] neg_hi:[0,1]
	v_pk_add_f32 v[246:247], v[228:229], v[246:247] neg_lo:[0,1] neg_hi:[0,1]
	v_pk_add_f32 v[248:249], v[230:231], v[248:249] neg_lo:[0,1] neg_hi:[0,1]
	v_cvt_pk_bf16_f32 v54, v242, v243
	v_cvt_pk_bf16_f32 v55, v244, v245
	v_cvt_pk_bf16_f32 v56, v246, v247
	v_cvt_pk_bf16_f32 v57, v248, v249
	s_waitcnt vmcnt(20)
	v_cvt_pk_bf16_f32 v42, v232, v233
	v_cvt_pk_bf16_f32 v43, v234, v235
	v_cvt_pk_bf16_f32 v44, v236, v237
	v_cvt_pk_bf16_f32 v45, v238, v239
	v_lshlrev_b32_e32 v242, 16, v42
	v_and_b32_e32 v243, 0xffff0000, v42
	v_lshlrev_b32_e32 v244, 16, v43
	v_and_b32_e32 v245, 0xffff0000, v43
	v_lshlrev_b32_e32 v246, 16, v44
	v_and_b32_e32 v247, 0xffff0000, v44
	v_lshlrev_b32_e32 v248, 16, v45
	v_and_b32_e32 v249, 0xffff0000, v45
	v_pk_add_f32 v[242:243], v[232:233], v[242:243] neg_lo:[0,1] neg_hi:[0,1]
	v_pk_add_f32 v[244:245], v[234:235], v[244:245] neg_lo:[0,1] neg_hi:[0,1]
	v_pk_add_f32 v[246:247], v[236:237], v[246:247] neg_lo:[0,1] neg_hi:[0,1]
	v_pk_add_f32 v[248:249], v[238:239], v[248:249] neg_lo:[0,1] neg_hi:[0,1]
	v_cvt_pk_bf16_f32 v46, v242, v243
	v_cvt_pk_bf16_f32 v47, v244, v245
	v_cvt_pk_bf16_f32 v48, v246, v247
	v_cvt_pk_bf16_f32 v49, v248, v249
	s_waitcnt vmcnt(13)
	ds_write_b128 v200, v[158:161]
	ds_write_b128 v200, v[122:125] offset:1152
	ds_write_b128 v200, v[126:129] offset:2304
	ds_write_b128 v200, v[132:135] offset:3456
	v_add3_u32 v197, v84, v86, v82
	ds_read_b128 v[90:93], v197
	ds_read_b128 v[94:97], v197 offset:64
	ds_read_b128 v[132:135], v197 offset:128
	ds_read_b128 v[158:161], v197 offset:192
	v_lshrrev_b32_e32 v82, 2, v130
	v_and_b32_e32 v84, 3, v0
	v_cmp_eq_u32_e32 vcc, v83, v82
	v_or_b32_e32 v196, 0x800, v0
	s_nop 0
	v_cndmask_b32_e32 v82, 4, v84, vcc
	v_cmp_eq_u32_e64 s[6:7], 0, v82
	v_cmp_eq_u32_e64 s[4:5], 1, v82
	v_cmp_eq_u32_e64 s[2:3], 2, v82
	v_cmp_eq_u32_e32 vcc, 3, v82
	s_mov_b32 s18, 0x3e8100
	s_mov_b32 s19, 0x465100
	buffer_load_dwordx4 v[82:85], v201, s[8:11], s18 offen nt
	buffer_load_dwordx4 v[86:89], v201, s[8:11], s19 offen nt
	s_mov_b32 s18, 0x4e2100
	s_mov_b32 s19, 0x55f100
	buffer_load_dwordx4 v[122:125], v201, s[8:11], s18 offen nt
	buffer_load_dwordx4 v[126:129], v201, s[8:11], s19 offen nt
	ds_write_b128 v200, v[136:139] offset:4608
	ds_write_b128 v200, v[140:143] offset:5760
	ds_write_b128 v200, v[154:157] offset:6912
	s_waitcnt vmcnt(15)
	ds_write_b128 v200, v[162:165] offset:8064
	s_waitcnt lgkmcnt(7)
	v_cvt_pk_bf16_f32 v136, v90, v91
	v_cvt_pk_bf16_f32 v137, v92, v93
	s_waitcnt lgkmcnt(6)
	v_cvt_pk_bf16_f32 v138, v94, v95
	v_cvt_pk_bf16_f32 v139, v96, v97
	v_lshlrev_b32_e32 v144, 16, v136
	v_and_b32_e32 v145, 0xffff0000, v136
	v_mfma_f32_16x16x32_bf16 v[140:143], v[22:25], v[136:139], 0
	v_add_f32_e64 v90, v90, -v144
	v_add_f32_e64 v91, v91, -v145
	v_lshlrev_b32_e32 v144, 16, v137
	v_and_b32_e32 v145, 0xffff0000, v137
	v_mfma_f32_16x16x32_bf16 v[154:157], v[34:37], v[136:139], 0
	v_add_f32_e64 v92, v92, -v144
	v_add_f32_e64 v93, v93, -v145
	v_cvt_pk_bf16_f32 v90, v90, v91
	v_cvt_pk_bf16_f32 v91, v92, v93
	v_lshlrev_b32_e32 v92, 16, v138
	v_and_b32_e32 v93, 0xffff0000, v138
	v_mfma_f32_16x16x32_bf16 v[140:143], v[30:33], v[136:139], v[140:143]
	v_add_f32_e64 v92, v94, -v92
	v_add_f32_e64 v93, v95, -v93
	v_lshlrev_b32_e32 v94, 16, v139
	v_and_b32_e32 v95, 0xffff0000, v139
	v_mfma_f32_16x16x32_bf16 v[154:157], v[38:41], v[136:139], v[154:157]
	v_add_f32_e64 v94, v96, -v94
	v_add_f32_e64 v95, v97, -v95
	v_cvt_pk_bf16_f32 v92, v92, v93
	v_cvt_pk_bf16_f32 v93, v94, v95
	v_mfma_f32_16x16x32_bf16 v[162:165], v[136:139], v[136:139], 0
	v_lshl_or_b32 v199, v1, 8, v130
	v_cndmask_b32_e64 v130, v196, v199, s[6:7]
	v_mov_b32_e32 v198, 0x20000
	v_mfma_f32_16x16x32_bf16 v[94:97], v[136:139], v[90:93], 0
	v_lshl_or_b32 v130, v130, 2, v198
	v_mfma_f32_16x16x32_bf16 v[136:139], v[22:25], v[90:93], v[140:143]
	v_mfma_f32_16x16x32_bf16 v[90:93], v[34:37], v[90:93], v[154:157]
	s_waitcnt lgkmcnt(5)
	s_nop 0
	v_cvt_pk_bf16_f32 v140, v132, v133
	v_lshlrev_b32_e32 v142, 16, v140
	v_and_b32_e32 v143, 0xffff0000, v140
	v_pk_add_f32 v[132:133], v[132:133], v[142:143] neg_lo:[0,1] neg_hi:[0,1]
	v_cvt_pk_bf16_f32 v141, v134, v135
	s_waitcnt lgkmcnt(4)
	v_cvt_pk_bf16_f32 v142, v158, v159
	v_cvt_pk_bf16_f32 v143, v160, v161
	v_lshlrev_b32_e32 v144, 16, v141
	v_and_b32_e32 v145, 0xffff0000, v141
	v_mfma_f32_16x16x32_bf16 v[90:93], v[66:69], v[140:143], v[90:93]
	v_add_f32_e64 v134, v134, -v144
	v_add_f32_e64 v135, v135, -v145
	v_cvt_pk_bf16_f32 v132, v132, v133
	v_cvt_pk_bf16_f32 v133, v134, v135
	v_lshlrev_b32_e32 v134, 16, v142
	v_and_b32_e32 v135, 0xffff0000, v142
	v_lshlrev_b32_e32 v144, 16, v143
	v_and_b32_e32 v145, 0xffff0000, v143
	v_pk_add_f32 v[134:135], v[158:159], v[134:135] neg_lo:[0,1] neg_hi:[0,1]
	v_pk_add_f32 v[144:145], v[160:161], v[144:145] neg_lo:[0,1] neg_hi:[0,1]
	v_mfma_f32_16x16x32_bf16 v[136:139], v[18:21], v[140:143], v[136:139]
	v_cvt_pk_bf16_f32 v134, v134, v135
	v_cvt_pk_bf16_f32 v135, v144, v145
	v_mfma_f32_16x16x32_bf16 v[90:93], v[70:73], v[140:143], v[90:93]
	v_mfma_f32_16x16x32_bf16 v[154:157], v[140:143], v[140:143], v[162:165]
	v_mfma_f32_16x16x32_bf16 v[94:97], v[140:143], v[132:135], v[94:97]
	v_mfma_f32_16x16x32_bf16 v[136:139], v[26:29], v[140:143], v[136:139]
	v_mfma_f32_16x16x32_bf16 v[142:145], v[66:69], v[132:135], v[90:93]
	s_nop 5
	v_fma_f32 v94, v94, 2.0, v154
	v_fma_f32 v95, v95, 2.0, v155
	ds_write_b32 v130, v94
	v_pk_fma_f32 v[96:97], v[96:97], 2.0, v[156:157] op_sel_hi:[1,0,1]
	v_cndmask_b32_e64 v90, v196, v199, s[4:5]
	v_lshl_or_b32 v90, v90, 2, v198
	ds_write_b32 v90, v95
	v_cndmask_b32_e64 v90, v196, v199, s[2:3]
	v_lshl_or_b32 v90, v90, 2, v198
	ds_write_b32 v90, v96
	v_cndmask_b32_e32 v90, v196, v199, vcc
	v_lshl_or_b32 v90, v90, 2, v198
	v_mfma_f32_16x16x32_bf16 v[138:141], v[18:21], v[132:135], v[136:139]
	ds_write_b32 v90, v97
	ds_read_b128 v[154:157], v197 offset:4608
	ds_read_b128 v[158:161], v197 offset:4672
	ds_read_b128 v[162:165], v197 offset:4736
	ds_read_b128 v[166:169], v197 offset:4800
	s_mov_b32 s18, 0x5dc000
	s_mov_b32 s19, 0x659000
	buffer_load_dwordx4 v[90:93], v201, s[8:11], s18 offen nt
	buffer_load_dwordx4 v[94:97], v201, s[8:11], s19 offen nt
	s_mov_b32 s18, 0x6d6000
	s_mov_b32 s19, 0x753000
	buffer_load_dwordx4 v[130:133], v201, s[8:11], s18 offen nt
	buffer_load_dwordx4 v[134:137], v201, s[8:11], s19 offen nt
	ds_write_b128 v200, v[58:61]
	s_waitcnt vmcnt(18)
	ds_write_b128 v200, v[62:65] offset:1152
	s_waitcnt vmcnt(17)
	ds_write_b128 v200, v[98:101] offset:2304
	s_waitcnt vmcnt(16)
	ds_write_b128 v200, v[102:105] offset:3456
	s_waitcnt lgkmcnt(7)
	v_cvt_pk_bf16_f32 v58, v154, v155
	v_cvt_pk_bf16_f32 v59, v156, v157
	s_waitcnt lgkmcnt(6)
	v_cvt_pk_bf16_f32 v60, v158, v159
	v_cvt_pk_bf16_f32 v61, v160, v161
	v_lshlrev_b32_e32 v98, 16, v58
	v_and_b32_e32 v99, 0xffff0000, v58
	v_mfma_f32_16x16x32_bf16 v[62:65], v[6:9], v[58:61], v[138:141]
	v_lshlrev_b32_e32 v100, 16, v59
	v_and_b32_e32 v101, 0xffff0000, v59
	v_pk_add_f32 v[98:99], v[154:155], v[98:99] neg_lo:[0,1] neg_hi:[0,1]
	v_mfma_f32_16x16x32_bf16 v[102:105], v[50:53], v[58:61], v[142:145]
	v_add_f32_e64 v100, v156, -v100
	v_add_f32_e64 v101, v157, -v101
	v_cvt_pk_bf16_f32 v98, v98, v99
	v_cvt_pk_bf16_f32 v99, v100, v101
	v_mfma_f32_16x16x32_bf16 v[62:65], v[14:17], v[58:61], v[62:65]
	v_lshlrev_b32_e32 v100, 16, v60
	v_and_b32_e32 v101, 0xffff0000, v60
	v_lshlrev_b32_e32 v142, 16, v61
	v_and_b32_e32 v143, 0xffff0000, v61
	v_pk_add_f32 v[100:101], v[158:159], v[100:101] neg_lo:[0,1] neg_hi:[0,1]
	v_mfma_f32_16x16x32_bf16 v[102:105], v[54:57], v[58:61], v[102:105]
	v_add_f32_e64 v142, v160, -v142
	v_add_f32_e64 v143, v161, -v143
	v_cvt_pk_bf16_f32 v100, v100, v101
	v_cvt_pk_bf16_f32 v101, v142, v143
	s_waitcnt lgkmcnt(5)
	v_cvt_pk_bf16_f32 v142, v162, v163
	v_mfma_f32_16x16x32_bf16 v[138:141], v[58:61], v[58:61], 0
	v_lshlrev_b32_e32 v144, 16, v142
	v_and_b32_e32 v145, 0xffff0000, v142
	v_cvt_pk_bf16_f32 v143, v164, v165
	v_mfma_f32_16x16x32_bf16 v[62:65], v[6:9], v[98:101], v[62:65]
	v_mfma_f32_16x16x32_bf16 v[58:61], v[58:61], v[98:101], 0
	v_mfma_f32_16x16x32_bf16 v[98:101], v[50:53], v[98:101], v[102:105]
	s_nop 2
	v_add_f32_e64 v102, v162, -v144
	v_add_f32_e64 v103, v163, -v145
	s_waitcnt lgkmcnt(4)
	v_cvt_pk_bf16_f32 v144, v166, v167
	v_cvt_pk_bf16_f32 v145, v168, v169
	v_lshlrev_b32_e32 v104, 16, v143
	v_and_b32_e32 v105, 0xffff0000, v143
	v_mfma_f32_16x16x32_bf16 v[62:65], v[2:5], v[142:145], v[62:65]
	v_add_f32_e64 v104, v164, -v104
	v_add_f32_e64 v105, v165, -v105
	v_cvt_pk_bf16_f32 v102, v102, v103
	v_cvt_pk_bf16_f32 v103, v104, v105
	v_lshlrev_b32_e32 v104, 16, v144
	v_and_b32_e32 v105, 0xffff0000, v144
	v_lshlrev_b32_e32 v154, 16, v145
	v_and_b32_e32 v155, 0xffff0000, v145
	v_mfma_f32_16x16x32_bf16 v[98:101], v[42:45], v[142:145], v[98:101]
	v_add_f32_e64 v104, v166, -v104
	v_add_f32_e64 v105, v167, -v105
	v_pk_add_f32 v[154:155], v[168:169], v[154:155] neg_lo:[0,1] neg_hi:[0,1]
	v_cvt_pk_bf16_f32 v104, v104, v105
	v_cvt_pk_bf16_f32 v105, v154, v155
	v_mfma_f32_16x16x32_bf16 v[138:141], v[142:145], v[142:145], v[138:141]
	v_mfma_f32_16x16x32_bf16 v[62:65], v[10:13], v[142:145], v[62:65]
	v_mfma_f32_16x16x32_bf16 v[58:61], v[142:145], v[102:105], v[58:61]
	v_mfma_f32_16x16x32_bf16 v[98:101], v[46:49], v[142:145], v[98:101]
	v_or_b32_e32 v142, 0x80, v199
	v_cndmask_b32_e64 v143, v196, v142, s[6:7]
	s_nop 4
	v_pk_fma_f32 v[140:141], v[60:61], 2.0, v[140:141] op_sel_hi:[1,0,1]
	v_pk_fma_f32 v[138:139], v[58:59], 2.0, v[138:139] op_sel_hi:[1,0,1]
	v_mfma_f32_16x16x32_bf16 v[58:61], v[2:5], v[102:105], v[62:65]
	s_nop 2
	v_lshl_or_b32 v62, v143, 2, v198
	ds_write_b32 v62, v138
	v_cndmask_b32_e64 v138, v196, v142, s[4:5]
	v_mfma_f32_16x16x32_bf16 v[62:65], v[42:45], v[102:105], v[98:101]
	s_nop 2
	v_lshl_or_b32 v98, v138, 2, v198
	ds_write_b32 v98, v139
	v_cndmask_b32_e64 v98, v196, v142, s[2:3]
	v_lshl_or_b32 v98, v98, 2, v198
	ds_write_b32 v98, v140
	v_cndmask_b32_e32 v98, v196, v142, vcc
	v_lshl_or_b32 v98, v98, 2, v198
	ds_write_b32 v98, v141
	ds_read_b128 v[154:157], v197
	ds_read_b128 v[158:161], v197 offset:64
	ds_read_b128 v[162:165], v197 offset:128
	ds_read_b128 v[166:169], v197 offset:192
	s_mov_b32 s18, 0x5dc100
	s_mov_b32 s19, 0x659100
	buffer_load_dwordx4 v[98:101], v201, s[8:11], s18 offen nt
	buffer_load_dwordx4 v[102:105], v201, s[8:11], s19 offen nt
	s_mov_b32 s18, 0x6d6100
	s_mov_b32 s19, 0x753100
	buffer_load_dwordx4 v[138:141], v201, s[8:11], s18 offen nt
	buffer_load_dwordx4 v[142:145], v201, s[8:11], s19 offen nt
	s_waitcnt vmcnt(19)
	ds_write_b128 v200, v[106:109] offset:4608
	s_waitcnt vmcnt(18)
	ds_write_b128 v200, v[110:113] offset:5760
	s_waitcnt vmcnt(17)
	ds_write_b128 v200, v[146:149] offset:6912
	s_waitcnt vmcnt(16)
	ds_write_b128 v200, v[150:153] offset:8064
	s_waitcnt lgkmcnt(7)
	v_cvt_pk_bf16_f32 v106, v154, v155
	v_cvt_pk_bf16_f32 v107, v156, v157
	s_waitcnt lgkmcnt(6)
	v_cvt_pk_bf16_f32 v108, v158, v159
	v_cvt_pk_bf16_f32 v109, v160, v161
	v_lshlrev_b32_e32 v146, 16, v106
	v_and_b32_e32 v147, 0xffff0000, v106
	v_mfma_f32_16x16x32_bf16 v[110:113], v[22:25], v[106:109], 0
	v_lshlrev_b32_e32 v148, 16, v107
	v_and_b32_e32 v149, 0xffff0000, v107
	v_pk_add_f32 v[146:147], v[154:155], v[146:147] neg_lo:[0,1] neg_hi:[0,1]
	v_mfma_f32_16x16x32_bf16 v[150:153], v[34:37], v[106:109], 0
	v_add_f32_e64 v148, v156, -v148
	v_add_f32_e64 v149, v157, -v149
	v_cvt_pk_bf16_f32 v146, v146, v147
	v_cvt_pk_bf16_f32 v147, v148, v149
	v_lshlrev_b32_e32 v148, 16, v108
	v_and_b32_e32 v149, 0xffff0000, v108
	v_mfma_f32_16x16x32_bf16 v[110:113], v[30:33], v[106:109], v[110:113]
	v_add_f32_e64 v148, v158, -v148
	v_add_f32_e64 v149, v159, -v149
	v_lshlrev_b32_e32 v158, 16, v109
	v_and_b32_e32 v159, 0xffff0000, v109
	v_pk_add_f32 v[158:159], v[160:161], v[158:159] neg_lo:[0,1] neg_hi:[0,1]
	v_cvt_pk_bf16_f32 v148, v148, v149
	v_mfma_f32_16x16x32_bf16 v[150:153], v[38:41], v[106:109], v[150:153]
	v_cvt_pk_bf16_f32 v149, v158, v159
	s_waitcnt lgkmcnt(5)
	v_cvt_pk_bf16_f32 v158, v162, v163
	v_lshlrev_b32_e32 v160, 16, v158
	v_mfma_f32_16x16x32_bf16 v[110:113], v[22:25], v[146:149], v[110:113]
	v_and_b32_e32 v161, 0xffff0000, v158
	v_cvt_pk_bf16_f32 v159, v164, v165
	v_mfma_f32_16x16x32_bf16 v[154:157], v[106:109], v[106:109], 0
	v_mfma_f32_16x16x32_bf16 v[106:109], v[106:109], v[146:149], 0
	v_mfma_f32_16x16x32_bf16 v[146:149], v[34:37], v[146:149], v[150:153]
	s_nop 2
	v_add_f32_e64 v150, v162, -v160
	v_add_f32_e64 v151, v163, -v161
	s_waitcnt lgkmcnt(4)
	v_cvt_pk_bf16_f32 v160, v166, v167
	v_cvt_pk_bf16_f32 v161, v168, v169
	v_lshlrev_b32_e32 v152, 16, v159
	v_and_b32_e32 v153, 0xffff0000, v159
	v_mfma_f32_16x16x32_bf16 v[110:113], v[18:21], v[158:161], v[110:113]
	v_add_f32_e64 v152, v164, -v152
	v_add_f32_e64 v153, v165, -v153
	v_cvt_pk_bf16_f32 v150, v150, v151
	v_cvt_pk_bf16_f32 v151, v152, v153
	v_lshlrev_b32_e32 v152, 16, v160
	v_and_b32_e32 v153, 0xffff0000, v160
	v_lshlrev_b32_e32 v162, 16, v161
	v_and_b32_e32 v163, 0xffff0000, v161
	v_pk_add_f32 v[152:153], v[166:167], v[152:153] neg_lo:[0,1] neg_hi:[0,1]
	v_pk_add_f32 v[162:163], v[168:169], v[162:163] neg_lo:[0,1] neg_hi:[0,1]
	v_mfma_f32_16x16x32_bf16 v[146:149], v[66:69], v[158:161], v[146:149]
	v_cvt_pk_bf16_f32 v152, v152, v153
	v_cvt_pk_bf16_f32 v153, v162, v163
	v_or_b32_e32 v162, 16, v199
	v_mfma_f32_16x16x32_bf16 v[154:157], v[158:161], v[158:161], v[154:157]
	v_mfma_f32_16x16x32_bf16 v[110:113], v[26:29], v[158:161], v[110:113]
	v_mfma_f32_16x16x32_bf16 v[106:109], v[158:161], v[150:153], v[106:109]
	v_mfma_f32_16x16x32_bf16 v[146:149], v[70:73], v[158:161], v[146:149]
	v_cndmask_b32_e64 v158, v196, v162, s[6:7]
	s_nop 5
	v_pk_fma_f32 v[108:109], v[108:109], 2.0, v[156:157] op_sel_hi:[1,0,1]
	v_pk_fma_f32 v[106:107], v[106:107], 2.0, v[154:155] op_sel_hi:[1,0,1]
	v_mfma_f32_16x16x32_bf16 v[154:157], v[18:21], v[150:153], v[110:113]
	s_nop 2
	v_lshl_or_b32 v110, v158, 2, v198
	ds_write_b32 v110, v106
	v_cndmask_b32_e64 v106, v196, v162, s[4:5]
	v_lshl_or_b32 v106, v106, 2, v198
	ds_write_b32 v106, v107
	v_cndmask_b32_e64 v106, v196, v162, s[2:3]
	v_lshl_or_b32 v106, v106, 2, v198
	ds_write_b32 v106, v108
	v_cndmask_b32_e32 v106, v196, v162, vcc
	v_lshl_or_b32 v106, v106, 2, v198
	v_mfma_f32_16x16x32_bf16 v[158:161], v[66:69], v[150:153], v[146:149]
	ds_write_b32 v106, v109
	ds_read_b128 v[162:165], v197 offset:4608
	ds_read_b128 v[166:169], v197 offset:4672
	ds_read_b128 v[170:173], v197 offset:4736
	ds_read_b128 v[174:177], v197 offset:4800
	s_mov_b32 s18, 0x7d0000
	s_mov_b32 s19, 0x84d000
	buffer_load_dwordx4 v[106:109], v201, s[8:11], s18 offen nt
	buffer_load_dwordx4 v[110:113], v201, s[8:11], s19 offen nt
	s_mov_b32 s18, 0x8ca000
	s_mov_b32 s19, 0x947000
	buffer_load_dwordx4 v[146:149], v201, s[8:11], s18 offen nt
	buffer_load_dwordx4 v[150:153], v201, s[8:11], s19 offen nt
	s_waitcnt vmcnt(19)
	ds_write_b128 v200, v[74:77]
	s_waitcnt vmcnt(18)
	ds_write_b128 v200, v[78:81] offset:1152
	s_waitcnt vmcnt(17)
	ds_write_b128 v200, v[114:117] offset:2304
	s_waitcnt vmcnt(16)
	ds_write_b128 v200, v[118:121] offset:3456
	s_waitcnt lgkmcnt(7)
	v_cvt_pk_bf16_f32 v74, v162, v163
	v_cvt_pk_bf16_f32 v75, v164, v165
	s_waitcnt lgkmcnt(6)
	v_cvt_pk_bf16_f32 v76, v166, v167
	v_cvt_pk_bf16_f32 v77, v168, v169
	v_lshlrev_b32_e32 v114, 16, v74
	v_and_b32_e32 v115, 0xffff0000, v74
	v_mfma_f32_16x16x32_bf16 v[78:81], v[6:9], v[74:77], v[154:157]
	v_lshlrev_b32_e32 v116, 16, v75
	v_and_b32_e32 v117, 0xffff0000, v75
	v_pk_add_f32 v[114:115], v[162:163], v[114:115] neg_lo:[0,1] neg_hi:[0,1]
	v_mfma_f32_16x16x32_bf16 v[118:121], v[50:53], v[74:77], v[158:161]
	v_add_f32_e64 v116, v164, -v116
	v_add_f32_e64 v117, v165, -v117
	v_cvt_pk_bf16_f32 v114, v114, v115
	v_cvt_pk_bf16_f32 v115, v116, v117
	v_mfma_f32_16x16x32_bf16 v[78:81], v[14:17], v[74:77], v[78:81]
	v_lshlrev_b32_e32 v116, 16, v76
	v_and_b32_e32 v117, 0xffff0000, v76
	v_lshlrev_b32_e32 v158, 16, v77
	v_and_b32_e32 v159, 0xffff0000, v77
	v_pk_add_f32 v[116:117], v[166:167], v[116:117] neg_lo:[0,1] neg_hi:[0,1]
	v_mfma_f32_16x16x32_bf16 v[118:121], v[54:57], v[74:77], v[118:121]
	v_add_f32_e64 v158, v168, -v158
	v_add_f32_e64 v159, v169, -v159
	v_cvt_pk_bf16_f32 v116, v116, v117
	v_cvt_pk_bf16_f32 v117, v158, v159
	s_waitcnt lgkmcnt(5)
	v_cvt_pk_bf16_f32 v158, v170, v171
	v_mfma_f32_16x16x32_bf16 v[154:157], v[74:77], v[74:77], 0
	v_lshlrev_b32_e32 v160, 16, v158
	v_and_b32_e32 v161, 0xffff0000, v158
	v_cvt_pk_bf16_f32 v159, v172, v173
	v_mfma_f32_16x16x32_bf16 v[78:81], v[6:9], v[114:117], v[78:81]
	v_mfma_f32_16x16x32_bf16 v[74:77], v[74:77], v[114:117], 0
	v_mfma_f32_16x16x32_bf16 v[114:117], v[50:53], v[114:117], v[118:121]
	s_nop 2
	v_add_f32_e64 v118, v170, -v160
	v_add_f32_e64 v119, v171, -v161
	s_waitcnt lgkmcnt(4)
	v_cvt_pk_bf16_f32 v160, v174, v175
	v_cvt_pk_bf16_f32 v161, v176, v177
	v_lshlrev_b32_e32 v120, 16, v159
	v_and_b32_e32 v121, 0xffff0000, v159
	v_mfma_f32_16x16x32_bf16 v[78:81], v[2:5], v[158:161], v[78:81]
	v_add_f32_e64 v120, v172, -v120
	v_add_f32_e64 v121, v173, -v121
	v_cvt_pk_bf16_f32 v118, v118, v119
	v_cvt_pk_bf16_f32 v119, v120, v121
	v_lshlrev_b32_e32 v120, 16, v160
	v_and_b32_e32 v121, 0xffff0000, v160
	v_lshlrev_b32_e32 v162, 16, v161
	v_and_b32_e32 v163, 0xffff0000, v161
	v_mfma_f32_16x16x32_bf16 v[114:117], v[42:45], v[158:161], v[114:117]
	v_add_f32_e64 v120, v174, -v120
	v_add_f32_e64 v121, v175, -v121
	v_pk_add_f32 v[162:163], v[176:177], v[162:163] neg_lo:[0,1] neg_hi:[0,1]
	v_cvt_pk_bf16_f32 v120, v120, v121
	v_cvt_pk_bf16_f32 v121, v162, v163
	v_mfma_f32_16x16x32_bf16 v[154:157], v[158:161], v[158:161], v[154:157]
	v_mfma_f32_16x16x32_bf16 v[78:81], v[10:13], v[158:161], v[78:81]
	v_mfma_f32_16x16x32_bf16 v[74:77], v[158:161], v[118:121], v[74:77]
	v_mfma_f32_16x16x32_bf16 v[114:117], v[46:49], v[158:161], v[114:117]
	v_or_b32_e32 v158, 0x90, v199
	v_cndmask_b32_e64 v159, v196, v158, s[6:7]
	s_nop 4
	v_pk_fma_f32 v[156:157], v[76:77], 2.0, v[156:157] op_sel_hi:[1,0,1]
	v_pk_fma_f32 v[154:155], v[74:75], 2.0, v[154:155] op_sel_hi:[1,0,1]
	v_mfma_f32_16x16x32_bf16 v[74:77], v[2:5], v[118:121], v[78:81]
	s_nop 2
	v_lshl_or_b32 v78, v159, 2, v198
	ds_write_b32 v78, v154
	v_cndmask_b32_e64 v154, v196, v158, s[4:5]
	v_mfma_f32_16x16x32_bf16 v[78:81], v[42:45], v[118:121], v[114:117]
	s_nop 2
	v_lshl_or_b32 v114, v154, 2, v198
	ds_write_b32 v114, v155
	v_cndmask_b32_e64 v114, v196, v158, s[2:3]
	v_lshl_or_b32 v114, v114, 2, v198
	ds_write_b32 v114, v156
	v_cndmask_b32_e32 v114, v196, v158, vcc
	v_lshl_or_b32 v114, v114, 2, v198
	ds_write_b32 v114, v157
	ds_read_b128 v[162:165], v197
	ds_read_b128 v[166:169], v197 offset:64
	ds_read_b128 v[170:173], v197 offset:128
	ds_read_b128 v[174:177], v197 offset:192
	s_mov_b32 s18, 0x7d0100
	s_mov_b32 s19, 0x84d100
	buffer_load_dwordx4 v[114:117], v201, s[8:11], s18 offen nt
	buffer_load_dwordx4 v[118:121], v201, s[8:11], s19 offen nt
	s_mov_b32 s18, 0x8ca100
	s_mov_b32 s19, 0x947100
	buffer_load_dwordx4 v[154:157], v201, s[8:11], s18 offen nt
	buffer_load_dwordx4 v[158:161], v201, s[8:11], s19 offen nt
	s_waitcnt vmcnt(19)
	ds_write_b128 v200, v[82:85] offset:4608
	s_waitcnt vmcnt(18)
	ds_write_b128 v200, v[86:89] offset:5760
	s_waitcnt vmcnt(17)
	ds_write_b128 v200, v[122:125] offset:6912
	s_waitcnt vmcnt(16)
	ds_write_b128 v200, v[126:129] offset:8064
	s_waitcnt lgkmcnt(7)
	v_cvt_pk_bf16_f32 v82, v162, v163
	v_cvt_pk_bf16_f32 v83, v164, v165
	s_waitcnt lgkmcnt(6)
	v_cvt_pk_bf16_f32 v84, v166, v167
	v_cvt_pk_bf16_f32 v85, v168, v169
	v_lshlrev_b32_e32 v122, 16, v82
	v_and_b32_e32 v123, 0xffff0000, v82
	v_mfma_f32_16x16x32_bf16 v[86:89], v[22:25], v[82:85], 0
	v_lshlrev_b32_e32 v124, 16, v83
	v_and_b32_e32 v125, 0xffff0000, v83
	v_pk_add_f32 v[122:123], v[162:163], v[122:123] neg_lo:[0,1] neg_hi:[0,1]
	v_mfma_f32_16x16x32_bf16 v[126:129], v[34:37], v[82:85], 0
	v_add_f32_e64 v124, v164, -v124
	v_add_f32_e64 v125, v165, -v125
	v_cvt_pk_bf16_f32 v122, v122, v123
	v_cvt_pk_bf16_f32 v123, v124, v125
	v_lshlrev_b32_e32 v124, 16, v84
	v_and_b32_e32 v125, 0xffff0000, v84
	v_mfma_f32_16x16x32_bf16 v[86:89], v[30:33], v[82:85], v[86:89]
	v_add_f32_e64 v124, v166, -v124
	v_add_f32_e64 v125, v167, -v125
	v_lshlrev_b32_e32 v166, 16, v85
	v_and_b32_e32 v167, 0xffff0000, v85
	v_mfma_f32_16x16x32_bf16 v[126:129], v[38:41], v[82:85], v[126:129]
	v_add_f32_e64 v166, v168, -v166
	v_add_f32_e64 v167, v169, -v167
	v_cvt_pk_bf16_f32 v124, v124, v125
	v_cvt_pk_bf16_f32 v125, v166, v167
	s_waitcnt lgkmcnt(5)
	v_cvt_pk_bf16_f32 v166, v170, v171
	v_mfma_f32_16x16x32_bf16 v[162:165], v[82:85], v[82:85], 0
	v_lshlrev_b32_e32 v168, 16, v166
	v_and_b32_e32 v169, 0xffff0000, v166
	v_cvt_pk_bf16_f32 v167, v172, v173
	v_mfma_f32_16x16x32_bf16 v[86:89], v[22:25], v[122:125], v[86:89]
	v_mfma_f32_16x16x32_bf16 v[82:85], v[82:85], v[122:125], 0
	v_mfma_f32_16x16x32_bf16 v[122:125], v[34:37], v[122:125], v[126:129]
	s_nop 2
	v_add_f32_e64 v126, v170, -v168
	v_add_f32_e64 v127, v171, -v169
	s_waitcnt lgkmcnt(4)
	v_cvt_pk_bf16_f32 v168, v174, v175
	v_cvt_pk_bf16_f32 v169, v176, v177
	v_lshlrev_b32_e32 v128, 16, v167
	v_and_b32_e32 v129, 0xffff0000, v167
	v_mfma_f32_16x16x32_bf16 v[86:89], v[18:21], v[166:169], v[86:89]
	v_add_f32_e64 v128, v172, -v128
	v_add_f32_e64 v129, v173, -v129
	v_cvt_pk_bf16_f32 v126, v126, v127
	v_cvt_pk_bf16_f32 v127, v128, v129
	v_lshlrev_b32_e32 v128, 16, v168
	v_and_b32_e32 v129, 0xffff0000, v168
	v_lshlrev_b32_e32 v170, 16, v169
	v_and_b32_e32 v171, 0xffff0000, v169
	v_mfma_f32_16x16x32_bf16 v[122:125], v[66:69], v[166:169], v[122:125]
	v_add_f32_e64 v128, v174, -v128
	v_add_f32_e64 v129, v175, -v129
	v_pk_add_f32 v[170:171], v[176:177], v[170:171] neg_lo:[0,1] neg_hi:[0,1]
	v_cvt_pk_bf16_f32 v128, v128, v129
	v_cvt_pk_bf16_f32 v129, v170, v171
	v_mfma_f32_16x16x32_bf16 v[162:165], v[166:169], v[166:169], v[162:165]
	v_mfma_f32_16x16x32_bf16 v[86:89], v[26:29], v[166:169], v[86:89]
	v_mfma_f32_16x16x32_bf16 v[82:85], v[166:169], v[126:129], v[82:85]
	v_mfma_f32_16x16x32_bf16 v[122:125], v[70:73], v[166:169], v[122:125]
	v_or_b32_e32 v166, 32, v199
	v_cndmask_b32_e64 v167, v196, v166, s[6:7]
	s_nop 4
	v_pk_fma_f32 v[164:165], v[84:85], 2.0, v[164:165] op_sel_hi:[1,0,1]
	v_pk_fma_f32 v[162:163], v[82:83], 2.0, v[162:163] op_sel_hi:[1,0,1]
	v_mfma_f32_16x16x32_bf16 v[82:85], v[18:21], v[126:129], v[86:89]
	s_nop 2
	v_lshl_or_b32 v86, v167, 2, v198
	ds_write_b32 v86, v162
	v_cndmask_b32_e64 v162, v196, v166, s[4:5]
	v_mfma_f32_16x16x32_bf16 v[86:89], v[66:69], v[126:129], v[122:125]
	s_nop 2
	v_lshl_or_b32 v122, v162, 2, v198
	ds_write_b32 v122, v163
	v_cndmask_b32_e64 v122, v196, v166, s[2:3]
	v_lshl_or_b32 v122, v122, 2, v198
	ds_write_b32 v122, v164
	v_cndmask_b32_e32 v122, v196, v166, vcc
	v_lshl_or_b32 v122, v122, 2, v198
	ds_write_b32 v122, v165
	ds_read_b128 v[170:173], v197 offset:4608
	ds_read_b128 v[174:177], v197 offset:4672
	ds_read_b128 v[178:181], v197 offset:4736
	ds_read_b128 v[182:185], v197 offset:4800
	s_mov_b32 s18, 0x9c4000
	s_mov_b32 s19, 0xa41000
	buffer_load_dwordx4 v[122:125], v201, s[8:11], s18 offen nt
	buffer_load_dwordx4 v[126:129], v201, s[8:11], s19 offen nt
	s_mov_b32 s18, 0xabe000
	s_mov_b32 s19, 0xb3b000
	buffer_load_dwordx4 v[162:165], v201, s[8:11], s18 offen nt
	buffer_load_dwordx4 v[166:169], v201, s[8:11], s19 offen nt
	s_waitcnt vmcnt(19)
	ds_write_b128 v200, v[90:93]
	s_waitcnt vmcnt(18)
	ds_write_b128 v200, v[94:97] offset:1152
	s_waitcnt vmcnt(17)
	ds_write_b128 v200, v[130:133] offset:2304
	s_waitcnt vmcnt(16)
	ds_write_b128 v200, v[134:137] offset:3456
	s_waitcnt lgkmcnt(7)
	v_cvt_pk_bf16_f32 v90, v170, v171
	v_cvt_pk_bf16_f32 v91, v172, v173
	s_waitcnt lgkmcnt(6)
	v_cvt_pk_bf16_f32 v92, v174, v175
	v_cvt_pk_bf16_f32 v93, v176, v177
	v_lshlrev_b32_e32 v94, 16, v90
	v_and_b32_e32 v95, 0xffff0000, v90
	v_mfma_f32_16x16x32_bf16 v[82:85], v[6:9], v[90:93], v[82:85]
	v_lshlrev_b32_e32 v96, 16, v91
	v_and_b32_e32 v97, 0xffff0000, v91
	v_pk_add_f32 v[94:95], v[170:171], v[94:95] neg_lo:[0,1] neg_hi:[0,1]
	v_mfma_f32_16x16x32_bf16 v[86:89], v[50:53], v[90:93], v[86:89]
	v_add_f32_e64 v96, v172, -v96
	v_add_f32_e64 v97, v173, -v97
	v_cvt_pk_bf16_f32 v94, v94, v95
	v_cvt_pk_bf16_f32 v95, v96, v97
	v_lshlrev_b32_e32 v96, 16, v92
	v_and_b32_e32 v97, 0xffff0000, v92
	v_mfma_f32_16x16x32_bf16 v[82:85], v[14:17], v[90:93], v[82:85]
	v_lshlrev_b32_e32 v134, 16, v93
	v_and_b32_e32 v135, 0xffff0000, v93
	v_pk_add_f32 v[96:97], v[174:175], v[96:97] neg_lo:[0,1] neg_hi:[0,1]
	v_mfma_f32_16x16x32_bf16 v[86:89], v[54:57], v[90:93], v[86:89]
	v_add_f32_e64 v134, v176, -v134
	v_add_f32_e64 v135, v177, -v135
	v_cvt_pk_bf16_f32 v96, v96, v97
	v_cvt_pk_bf16_f32 v97, v134, v135
	s_waitcnt lgkmcnt(5)
	v_cvt_pk_bf16_f32 v134, v178, v179
	v_lshlrev_b32_e32 v136, 16, v134
	v_and_b32_e32 v137, 0xffff0000, v134
	v_cvt_pk_bf16_f32 v135, v180, v181
	v_mfma_f32_16x16x32_bf16 v[130:133], v[90:93], v[90:93], 0
	v_mfma_f32_16x16x32_bf16 v[90:93], v[90:93], v[94:97], 0
	v_mfma_f32_16x16x32_bf16 v[82:85], v[6:9], v[94:97], v[82:85]
	v_mfma_f32_16x16x32_bf16 v[86:89], v[50:53], v[94:97], v[86:89]
	v_add_f32_e64 v94, v178, -v136
	v_add_f32_e64 v95, v179, -v137
	s_waitcnt lgkmcnt(4)
	v_cvt_pk_bf16_f32 v136, v182, v183
	v_cvt_pk_bf16_f32 v137, v184, v185
	v_lshlrev_b32_e32 v96, 16, v135
	v_and_b32_e32 v97, 0xffff0000, v135
	v_pk_add_f32 v[96:97], v[180:181], v[96:97] neg_lo:[0,1] neg_hi:[0,1]
	v_cvt_pk_bf16_f32 v94, v94, v95
	v_cvt_pk_bf16_f32 v95, v96, v97
	v_lshlrev_b32_e32 v96, 16, v136
	v_and_b32_e32 v97, 0xffff0000, v136
	v_lshlrev_b32_e32 v170, 16, v137
	v_and_b32_e32 v171, 0xffff0000, v137
	v_pk_add_f32 v[96:97], v[182:183], v[96:97] neg_lo:[0,1] neg_hi:[0,1]
	v_pk_add_f32 v[170:171], v[184:185], v[170:171] neg_lo:[0,1] neg_hi:[0,1]
	v_cvt_pk_bf16_f32 v96, v96, v97
	v_cvt_pk_bf16_f32 v97, v170, v171
	v_mfma_f32_16x16x32_bf16 v[130:133], v[134:137], v[134:137], v[130:133]
	s_nop 0
	v_mfma_f32_16x16x32_bf16 v[90:93], v[134:137], v[94:97], v[90:93]
	v_mfma_f32_16x16x32_bf16 v[82:85], v[2:5], v[134:137], v[82:85]
	v_mfma_f32_16x16x32_bf16 v[86:89], v[42:45], v[134:137], v[86:89]
	s_nop 5
	v_fma_f32 v90, v90, 2.0, v130
	v_fma_f32 v91, v91, 2.0, v131
	v_or_b32_e32 v130, 0xa0, v199
	v_cndmask_b32_e64 v131, v196, v130, s[6:7]
	v_mfma_f32_16x16x32_bf16 v[82:85], v[10:13], v[134:137], v[82:85]
	v_lshl_or_b32 v131, v131, 2, v198
	ds_write_b32 v131, v90
	v_cndmask_b32_e64 v90, v196, v130, s[4:5]
	v_mfma_f32_16x16x32_bf16 v[86:89], v[46:49], v[134:137], v[86:89]
	v_lshl_or_b32 v90, v90, 2, v198
	ds_write_b32 v90, v91
	v_cndmask_b32_e64 v90, v196, v130, s[2:3]
	v_mfma_f32_16x16x32_bf16 v[82:85], v[2:5], v[94:97], v[82:85]
	v_fma_f32 v92, v92, 2.0, v132
	v_fma_f32 v93, v93, 2.0, v133
	v_lshl_or_b32 v90, v90, 2, v198
	ds_write_b32 v90, v92
	v_mfma_f32_16x16x32_bf16 v[86:89], v[42:45], v[94:97], v[86:89]
	v_cndmask_b32_e32 v90, v196, v130, vcc
	v_lshl_or_b32 v90, v90, 2, v198
	ds_write_b32 v90, v93
	ds_read_b128 v[90:93], v197
	ds_read_b128 v[94:97], v197 offset:64
	ds_read_b128 v[178:181], v197 offset:128
	ds_read_b128 v[182:185], v197 offset:192
	s_mov_b32 s18, 0x9c4100
	s_mov_b32 s19, 0xa41100
	buffer_load_dwordx4 v[130:133], v201, s[8:11], s18 offen nt
	buffer_load_dwordx4 v[134:137], v201, s[8:11], s19 offen nt
	s_mov_b32 s18, 0xabe100
	s_mov_b32 s19, 0xb3b100
	buffer_load_dwordx4 v[170:173], v201, s[8:11], s18 offen nt
	buffer_load_dwordx4 v[174:177], v201, s[8:11], s19 offen nt
	s_waitcnt vmcnt(19)
	ds_write_b128 v200, v[98:101] offset:4608
	s_waitcnt vmcnt(18)
	ds_write_b128 v200, v[102:105] offset:5760
	s_waitcnt vmcnt(17)
	ds_write_b128 v200, v[138:141] offset:6912
	s_waitcnt vmcnt(16)
	ds_write_b128 v200, v[142:145] offset:8064
	s_waitcnt lgkmcnt(7)
	v_cvt_pk_bf16_f32 v98, v90, v91
	v_cvt_pk_bf16_f32 v99, v92, v93
	s_waitcnt lgkmcnt(6)
	v_cvt_pk_bf16_f32 v100, v94, v95
	v_cvt_pk_bf16_f32 v101, v96, v97
	v_lshlrev_b32_e32 v138, 16, v98
	v_and_b32_e32 v139, 0xffff0000, v98
	v_mfma_f32_16x16x32_bf16 v[102:105], v[22:25], v[98:101], 0
	v_add_f32_e64 v90, v90, -v138
	v_add_f32_e64 v91, v91, -v139
	v_lshlrev_b32_e32 v142, 16, v99
	v_and_b32_e32 v143, 0xffff0000, v99
	v_mfma_f32_16x16x32_bf16 v[138:141], v[34:37], v[98:101], 0
	v_add_f32_e64 v92, v92, -v142
	v_add_f32_e64 v93, v93, -v143
	v_cvt_pk_bf16_f32 v90, v90, v91
	v_cvt_pk_bf16_f32 v91, v92, v93
	v_lshlrev_b32_e32 v92, 16, v100
	v_and_b32_e32 v93, 0xffff0000, v100
	v_mfma_f32_16x16x32_bf16 v[102:105], v[30:33], v[98:101], v[102:105]
	v_add_f32_e64 v92, v94, -v92
	v_add_f32_e64 v93, v95, -v93
	v_lshlrev_b32_e32 v94, 16, v101
	v_and_b32_e32 v95, 0xffff0000, v101
	v_mfma_f32_16x16x32_bf16 v[138:141], v[38:41], v[98:101], v[138:141]
	v_add_f32_e64 v94, v96, -v94
	v_add_f32_e64 v95, v97, -v95
	v_cvt_pk_bf16_f32 v92, v92, v93
	v_cvt_pk_bf16_f32 v93, v94, v95
	v_mfma_f32_16x16x32_bf16 v[142:145], v[98:101], v[98:101], 0
	s_nop 0
	v_mfma_f32_16x16x32_bf16 v[94:97], v[98:101], v[90:93], 0
	v_mfma_f32_16x16x32_bf16 v[98:101], v[22:25], v[90:93], v[102:105]
	s_waitcnt lgkmcnt(5)
	s_nop 1
	v_cvt_pk_bf16_f32 v102, v178, v179
	v_lshlrev_b32_e32 v104, 16, v102
	v_and_b32_e32 v105, 0xffff0000, v102
	v_mfma_f32_16x16x32_bf16 v[90:93], v[34:37], v[90:93], v[138:141]
	v_add_f32_e64 v104, v178, -v104
	v_add_f32_e64 v105, v179, -v105
	v_cvt_pk_bf16_f32 v103, v180, v181
	v_cvt_pk_bf16_f32 v138, v104, v105
	s_waitcnt lgkmcnt(4)
	v_cvt_pk_bf16_f32 v104, v182, v183
	v_cvt_pk_bf16_f32 v105, v184, v185
	v_lshlrev_b32_e32 v140, 16, v103
	v_and_b32_e32 v141, 0xffff0000, v103
	v_mfma_f32_16x16x32_bf16 v[98:101], v[18:21], v[102:105], v[98:101]
	v_add_f32_e64 v140, v180, -v140
	v_add_f32_e64 v141, v181, -v141
	v_lshlrev_b32_e32 v178, 16, v105
	v_cvt_pk_bf16_f32 v139, v140, v141
	v_lshlrev_b32_e32 v140, 16, v104
	v_and_b32_e32 v141, 0xffff0000, v104
	v_and_b32_e32 v179, 0xffff0000, v105
	v_mfma_f32_16x16x32_bf16 v[90:93], v[66:69], v[102:105], v[90:93]
	v_add_f32_e64 v140, v182, -v140
	v_add_f32_e64 v141, v183, -v141
	v_pk_add_f32 v[178:179], v[184:185], v[178:179] neg_lo:[0,1] neg_hi:[0,1]
	v_cvt_pk_bf16_f32 v140, v140, v141
	v_cvt_pk_bf16_f32 v141, v178, v179
	v_mfma_f32_16x16x32_bf16 v[142:145], v[102:105], v[102:105], v[142:145]
	v_mfma_f32_16x16x32_bf16 v[98:101], v[26:29], v[102:105], v[98:101]
	v_mfma_f32_16x16x32_bf16 v[94:97], v[102:105], v[138:141], v[94:97]
	v_mfma_f32_16x16x32_bf16 v[90:93], v[70:73], v[102:105], v[90:93]
	v_or_b32_e32 v104, 48, v199
	v_cndmask_b32_e64 v105, v196, v104, s[6:7]
	s_nop 4
	v_pk_fma_f32 v[144:145], v[96:97], 2.0, v[144:145] op_sel_hi:[1,0,1]
	v_pk_fma_f32 v[102:103], v[94:95], 2.0, v[142:143] op_sel_hi:[1,0,1]
	v_mfma_f32_16x16x32_bf16 v[94:97], v[18:21], v[138:141], v[98:101]
	s_nop 2
	v_lshl_or_b32 v98, v105, 2, v198
	ds_write_b32 v98, v102
	v_cndmask_b32_e64 v98, v196, v104, s[4:5]
	v_lshl_or_b32 v98, v98, 2, v198
	v_mfma_f32_16x16x32_bf16 v[90:93], v[66:69], v[138:141], v[90:93]
	ds_write_b32 v98, v103
	v_cndmask_b32_e64 v98, v196, v104, s[2:3]
	v_lshl_or_b32 v98, v98, 2, v198
	ds_write_b32 v98, v144
	v_cndmask_b32_e32 v98, v196, v104, vcc
	v_lshl_or_b32 v98, v98, 2, v198
	ds_write_b32 v98, v145
	ds_read_b128 v[98:101], v197 offset:4608
	ds_read_b128 v[102:105], v197 offset:4672
	ds_read_b128 v[186:189], v197 offset:4736
	ds_read_b128 v[190:193], v197 offset:4800
	s_mov_b32 s18, 0xbb8000
	s_mov_b32 s19, 0xc35000
	buffer_load_dwordx4 v[138:141], v201, s[8:11], s18 offen nt
	buffer_load_dwordx4 v[142:145], v201, s[8:11], s19 offen nt
	s_mov_b32 s18, 0xcb2000
	s_mov_b32 s19, 0xd2f000
	buffer_load_dwordx4 v[178:181], v201, s[8:11], s18 offen nt
	buffer_load_dwordx4 v[182:185], v201, s[8:11], s19 offen nt
	s_waitcnt vmcnt(19)
	ds_write_b128 v200, v[106:109]
	s_waitcnt vmcnt(18)
	ds_write_b128 v200, v[110:113] offset:1152
	s_waitcnt vmcnt(17)
	ds_write_b128 v200, v[146:149] offset:2304
	s_waitcnt vmcnt(16)
	ds_write_b128 v200, v[150:153] offset:3456
	s_waitcnt lgkmcnt(7)
	v_cvt_pk_bf16_f32 v106, v98, v99
	v_cvt_pk_bf16_f32 v107, v100, v101
	s_waitcnt lgkmcnt(6)
	v_cvt_pk_bf16_f32 v108, v102, v103
	v_cvt_pk_bf16_f32 v109, v104, v105
	v_lshlrev_b32_e32 v110, 16, v106
	v_and_b32_e32 v111, 0xffff0000, v106
	v_mfma_f32_16x16x32_bf16 v[94:97], v[6:9], v[106:109], v[94:97]
	v_add_f32_e64 v98, v98, -v110
	v_add_f32_e64 v99, v99, -v111
	v_lshlrev_b32_e32 v110, 16, v107
	v_and_b32_e32 v111, 0xffff0000, v107
	v_mfma_f32_16x16x32_bf16 v[90:93], v[50:53], v[106:109], v[90:93]
	v_add_f32_e64 v100, v100, -v110
	v_add_f32_e64 v101, v101, -v111
	v_cvt_pk_bf16_f32 v98, v98, v99
	v_cvt_pk_bf16_f32 v99, v100, v101
	v_lshlrev_b32_e32 v100, 16, v108
	v_and_b32_e32 v101, 0xffff0000, v108
	v_mfma_f32_16x16x32_bf16 v[94:97], v[14:17], v[106:109], v[94:97]
	v_add_f32_e64 v100, v102, -v100
	v_add_f32_e64 v101, v103, -v101
	v_lshlrev_b32_e32 v102, 16, v109
	v_and_b32_e32 v103, 0xffff0000, v109
	v_mfma_f32_16x16x32_bf16 v[90:93], v[54:57], v[106:109], v[90:93]
	v_add_f32_e64 v102, v104, -v102
	v_add_f32_e64 v103, v105, -v103
	v_cvt_pk_bf16_f32 v100, v100, v101
	v_cvt_pk_bf16_f32 v101, v102, v103
	v_mfma_f32_16x16x32_bf16 v[110:113], v[106:109], v[106:109], 0
	s_nop 0
	v_mfma_f32_16x16x32_bf16 v[102:105], v[106:109], v[98:101], 0
	s_waitcnt lgkmcnt(5)
	v_cvt_pk_bf16_f32 v106, v186, v187
	v_lshlrev_b32_e32 v108, 16, v106
	v_and_b32_e32 v109, 0xffff0000, v106
	v_mfma_f32_16x16x32_bf16 v[94:97], v[6:9], v[98:101], v[94:97]
	v_cvt_pk_bf16_f32 v107, v188, v189
	v_mfma_f32_16x16x32_bf16 v[90:93], v[50:53], v[98:101], v[90:93]
	v_add_f32_e64 v98, v186, -v108
	v_add_f32_e64 v99, v187, -v109
	s_waitcnt lgkmcnt(4)
	v_cvt_pk_bf16_f32 v108, v190, v191
	v_cvt_pk_bf16_f32 v109, v192, v193
	v_lshlrev_b32_e32 v100, 16, v107
	v_and_b32_e32 v101, 0xffff0000, v107
	v_pk_add_f32 v[100:101], v[188:189], v[100:101] neg_lo:[0,1] neg_hi:[0,1]
	v_cvt_pk_bf16_f32 v98, v98, v99
	v_cvt_pk_bf16_f32 v99, v100, v101
	v_lshlrev_b32_e32 v100, 16, v108
	v_and_b32_e32 v101, 0xffff0000, v108
	v_lshlrev_b32_e32 v146, 16, v109
	v_and_b32_e32 v147, 0xffff0000, v109
	v_mfma_f32_16x16x32_bf16 v[94:97], v[2:5], v[106:109], v[94:97]
	v_add_f32_e64 v100, v190, -v100
	v_add_f32_e64 v101, v191, -v101
	v_pk_add_f32 v[146:147], v[192:193], v[146:147] neg_lo:[0,1] neg_hi:[0,1]
	v_cvt_pk_bf16_f32 v100, v100, v101
	v_cvt_pk_bf16_f32 v101, v146, v147
	v_mfma_f32_16x16x32_bf16 v[90:93], v[42:45], v[106:109], v[90:93]
	v_mfma_f32_16x16x32_bf16 v[110:113], v[106:109], v[106:109], v[110:113]
	v_mfma_f32_16x16x32_bf16 v[102:105], v[106:109], v[98:101], v[102:105]
	v_mfma_f32_16x16x32_bf16 v[94:97], v[10:13], v[106:109], v[94:97]
	s_nop 6
	v_fma_f32 v112, v104, 2.0, v112
	v_fma_f32 v113, v105, 2.0, v113
	v_mfma_f32_16x16x32_bf16 v[104:107], v[46:49], v[106:109], v[90:93]
	v_or_b32_e32 v108, 0xb0, v199
	v_cndmask_b32_e64 v109, v196, v108, s[6:7]
	v_pk_fma_f32 v[102:103], v[102:103], 2.0, v[110:111] op_sel_hi:[1,0,1]
	v_mfma_f32_16x16x32_bf16 v[90:93], v[2:5], v[98:101], v[94:97]
	s_nop 2
	v_lshl_or_b32 v94, v109, 2, v198
	ds_write_b32 v94, v102
	v_cndmask_b32_e64 v102, v196, v108, s[4:5]
	v_mfma_f32_16x16x32_bf16 v[94:97], v[42:45], v[98:101], v[104:107]
	v_lshl_or_b32 v98, v102, 2, v198
	ds_write_b32 v98, v103
	v_cndmask_b32_e64 v98, v196, v108, s[2:3]
	v_lshl_or_b32 v98, v98, 2, v198
	ds_write_b32 v98, v112
	v_cndmask_b32_e32 v98, v196, v108, vcc
	v_lshl_or_b32 v98, v98, 2, v198
	ds_write_b32 v98, v113
	ds_read_b128 v[98:101], v197
	ds_read_b128 v[102:105], v197 offset:64
	ds_read_b128 v[106:109], v197 offset:128
	ds_read_b128 v[110:113], v197 offset:192
	s_mov_b32 s18, 0xbb8100
	s_mov_b32 s19, 0xc35100
	buffer_load_dwordx4 v[146:149], v201, s[8:11], s18 offen nt
	buffer_load_dwordx4 v[150:153], v201, s[8:11], s19 offen nt
	s_mov_b32 s18, 0xcb2100
	s_mov_b32 s19, 0xd2f100
	buffer_load_dwordx4 v[186:189], v201, s[8:11], s18 offen nt
	buffer_load_dwordx4 v[190:193], v201, s[8:11], s19 offen nt
	s_waitcnt vmcnt(19)
	ds_write_b128 v200, v[114:117] offset:4608
	s_waitcnt vmcnt(18)
	ds_write_b128 v200, v[118:121] offset:5760
	s_waitcnt vmcnt(17)
	ds_write_b128 v200, v[154:157] offset:6912
	s_waitcnt vmcnt(16)
	ds_write_b128 v200, v[158:161] offset:8064
	s_waitcnt lgkmcnt(7)
	v_cvt_pk_bf16_f32 v114, v98, v99
	v_cvt_pk_bf16_f32 v115, v100, v101
	s_waitcnt lgkmcnt(6)
	v_cvt_pk_bf16_f32 v116, v102, v103
	v_cvt_pk_bf16_f32 v117, v104, v105
	v_lshlrev_b32_e32 v154, 16, v114
	v_and_b32_e32 v155, 0xffff0000, v114
	v_mfma_f32_16x16x32_bf16 v[118:121], v[22:25], v[114:117], 0
	v_add_f32_e64 v98, v98, -v154
	v_add_f32_e64 v99, v99, -v155
	v_lshlrev_b32_e32 v158, 16, v115
	v_and_b32_e32 v159, 0xffff0000, v115
	v_mfma_f32_16x16x32_bf16 v[154:157], v[34:37], v[114:117], 0
	v_add_f32_e64 v100, v100, -v158
	v_add_f32_e64 v101, v101, -v159
	v_cvt_pk_bf16_f32 v98, v98, v99
	v_cvt_pk_bf16_f32 v99, v100, v101
	v_lshlrev_b32_e32 v100, 16, v116
	v_and_b32_e32 v101, 0xffff0000, v116
	v_mfma_f32_16x16x32_bf16 v[118:121], v[30:33], v[114:117], v[118:121]
	v_add_f32_e64 v100, v102, -v100
	v_add_f32_e64 v101, v103, -v101
	v_lshlrev_b32_e32 v102, 16, v117
	v_and_b32_e32 v103, 0xffff0000, v117
	v_mfma_f32_16x16x32_bf16 v[154:157], v[38:41], v[114:117], v[154:157]
	v_add_f32_e64 v102, v104, -v102
	v_add_f32_e64 v103, v105, -v103
	v_cvt_pk_bf16_f32 v100, v100, v101
	v_cvt_pk_bf16_f32 v101, v102, v103
	v_mfma_f32_16x16x32_bf16 v[158:161], v[114:117], v[114:117], 0
	s_nop 0
	v_mfma_f32_16x16x32_bf16 v[102:105], v[114:117], v[98:101], 0
	v_mfma_f32_16x16x32_bf16 v[114:117], v[22:25], v[98:101], v[118:121]
	s_waitcnt lgkmcnt(5)
	s_nop 1
	v_cvt_pk_bf16_f32 v118, v106, v107
	v_cvt_pk_bf16_f32 v119, v108, v109
	v_lshlrev_b32_e32 v120, 16, v118
	v_and_b32_e32 v121, 0xffff0000, v118
	v_mfma_f32_16x16x32_bf16 v[98:101], v[34:37], v[98:101], v[154:157]
	v_add_f32_e64 v106, v106, -v120
	v_add_f32_e64 v107, v107, -v121
	s_waitcnt lgkmcnt(4)
	v_cvt_pk_bf16_f32 v120, v110, v111
	v_cvt_pk_bf16_f32 v121, v112, v113
	v_lshlrev_b32_e32 v154, 16, v119
	v_and_b32_e32 v155, 0xffff0000, v119
	v_pk_add_f32 v[108:109], v[108:109], v[154:155] neg_lo:[0,1] neg_hi:[0,1]
	v_cvt_pk_bf16_f32 v106, v106, v107
	v_mfma_f32_16x16x32_bf16 v[114:117], v[18:21], v[118:121], v[114:117]
	v_cvt_pk_bf16_f32 v107, v108, v109
	v_lshlrev_b32_e32 v108, 16, v120
	v_and_b32_e32 v109, 0xffff0000, v120
	v_pk_add_f32 v[108:109], v[110:111], v[108:109] neg_lo:[0,1] neg_hi:[0,1]
	v_lshlrev_b32_e32 v110, 16, v121
	v_and_b32_e32 v111, 0xffff0000, v121
	v_mfma_f32_16x16x32_bf16 v[98:101], v[66:69], v[118:121], v[98:101]
	v_add_f32_e64 v110, v112, -v110
	v_add_f32_e64 v111, v113, -v111
	v_cvt_pk_bf16_f32 v108, v108, v109
	v_cvt_pk_bf16_f32 v109, v110, v111
	v_mfma_f32_16x16x32_bf16 v[154:157], v[118:121], v[118:121], v[158:161]
	v_mfma_f32_16x16x32_bf16 v[114:117], v[26:29], v[118:121], v[114:117]
	v_mfma_f32_16x16x32_bf16 v[102:105], v[118:121], v[106:109], v[102:105]
	v_mfma_f32_16x16x32_bf16 v[98:101], v[70:73], v[118:121], v[98:101]
	v_or_b32_e32 v118, 64, v199
	v_cndmask_b32_e64 v119, v196, v118, s[6:7]
	s_nop 4
	v_pk_fma_f32 v[110:111], v[104:105], 2.0, v[156:157] op_sel_hi:[1,0,1]
	v_pk_fma_f32 v[112:113], v[102:103], 2.0, v[154:155] op_sel_hi:[1,0,1]
	v_mfma_f32_16x16x32_bf16 v[102:105], v[18:21], v[106:109], v[114:117]
	s_nop 2
	v_lshl_or_b32 v114, v119, 2, v198
	ds_write_b32 v114, v112
	v_cndmask_b32_e64 v112, v196, v118, s[4:5]
	v_mfma_f32_16x16x32_bf16 v[98:101], v[66:69], v[106:109], v[98:101]
	v_lshl_or_b32 v106, v112, 2, v198
	ds_write_b32 v106, v113
	v_cndmask_b32_e64 v106, v196, v118, s[2:3]
	v_lshl_or_b32 v106, v106, 2, v198
	ds_write_b32 v106, v110
	v_cndmask_b32_e32 v106, v196, v118, vcc
	v_lshl_or_b32 v106, v106, 2, v198
	ds_write_b32 v106, v111
	ds_read_b128 v[106:109], v197 offset:4608
	ds_read_b128 v[110:113], v197 offset:4672
	ds_read_b128 v[202:205], v197 offset:4736
	ds_read_b128 v[206:209], v197 offset:4800
	s_mov_b32 s18, 0xdac000
	s_mov_b32 s19, 0xe29000
	buffer_load_dwordx4 v[114:117], v201, s[8:11], s18 offen nt
	buffer_load_dwordx4 v[118:121], v201, s[8:11], s19 offen nt
	s_mov_b32 s18, 0xea6000
	s_mov_b32 s19, 0xf23000
	buffer_load_dwordx4 v[154:157], v201, s[8:11], s18 offen nt
	buffer_load_dwordx4 v[158:161], v201, s[8:11], s19 offen nt
	s_waitcnt vmcnt(19)
	ds_write_b128 v200, v[122:125]
	s_waitcnt vmcnt(18)
	ds_write_b128 v200, v[126:129] offset:1152
	s_waitcnt vmcnt(17)
	ds_write_b128 v200, v[162:165] offset:2304
	s_waitcnt vmcnt(16)
	ds_write_b128 v200, v[166:169] offset:3456
	s_waitcnt lgkmcnt(7)
	v_cvt_pk_bf16_f32 v122, v106, v107
	v_cvt_pk_bf16_f32 v123, v108, v109
	s_waitcnt lgkmcnt(6)
	v_cvt_pk_bf16_f32 v124, v110, v111
	v_cvt_pk_bf16_f32 v125, v112, v113
	v_lshlrev_b32_e32 v126, 16, v122
	v_and_b32_e32 v127, 0xffff0000, v122
	v_mfma_f32_16x16x32_bf16 v[102:105], v[6:9], v[122:125], v[102:105]
	v_add_f32_e64 v106, v106, -v126
	v_add_f32_e64 v107, v107, -v127
	v_lshlrev_b32_e32 v126, 16, v123
	v_and_b32_e32 v127, 0xffff0000, v123
	v_mfma_f32_16x16x32_bf16 v[98:101], v[50:53], v[122:125], v[98:101]
	v_add_f32_e64 v108, v108, -v126
	v_add_f32_e64 v109, v109, -v127
	v_cvt_pk_bf16_f32 v106, v106, v107
	v_cvt_pk_bf16_f32 v107, v108, v109
	v_lshlrev_b32_e32 v108, 16, v124
	v_and_b32_e32 v109, 0xffff0000, v124
	v_mfma_f32_16x16x32_bf16 v[102:105], v[14:17], v[122:125], v[102:105]
	v_add_f32_e64 v108, v110, -v108
	v_add_f32_e64 v109, v111, -v109
	v_lshlrev_b32_e32 v110, 16, v125
	v_and_b32_e32 v111, 0xffff0000, v125
	v_mfma_f32_16x16x32_bf16 v[98:101], v[54:57], v[122:125], v[98:101]
	v_add_f32_e64 v110, v112, -v110
	v_add_f32_e64 v111, v113, -v111
	v_cvt_pk_bf16_f32 v108, v108, v109
	v_cvt_pk_bf16_f32 v109, v110, v111
	v_mfma_f32_16x16x32_bf16 v[126:129], v[122:125], v[122:125], 0
	s_nop 0
	v_mfma_f32_16x16x32_bf16 v[110:113], v[122:125], v[106:109], 0
	s_waitcnt lgkmcnt(5)
	v_cvt_pk_bf16_f32 v122, v202, v203
	v_lshlrev_b32_e32 v124, 16, v122
	v_and_b32_e32 v125, 0xffff0000, v122
	v_mfma_f32_16x16x32_bf16 v[102:105], v[6:9], v[106:109], v[102:105]
	v_cvt_pk_bf16_f32 v123, v204, v205
	v_mfma_f32_16x16x32_bf16 v[98:101], v[50:53], v[106:109], v[98:101]
	v_add_f32_e64 v106, v202, -v124
	v_add_f32_e64 v107, v203, -v125
	s_waitcnt lgkmcnt(4)
	v_cvt_pk_bf16_f32 v124, v206, v207
	v_cvt_pk_bf16_f32 v125, v208, v209
	v_lshlrev_b32_e32 v108, 16, v123
	v_and_b32_e32 v109, 0xffff0000, v123
	v_pk_add_f32 v[108:109], v[204:205], v[108:109] neg_lo:[0,1] neg_hi:[0,1]
	v_cvt_pk_bf16_f32 v106, v106, v107
	v_cvt_pk_bf16_f32 v107, v108, v109
	v_lshlrev_b32_e32 v108, 16, v124
	v_and_b32_e32 v109, 0xffff0000, v124
	v_lshlrev_b32_e32 v162, 16, v125
	v_and_b32_e32 v163, 0xffff0000, v125
	v_mfma_f32_16x16x32_bf16 v[102:105], v[2:5], v[122:125], v[102:105]
	v_add_f32_e64 v108, v206, -v108
	v_add_f32_e64 v109, v207, -v109
	v_pk_add_f32 v[162:163], v[208:209], v[162:163] neg_lo:[0,1] neg_hi:[0,1]
	v_cvt_pk_bf16_f32 v108, v108, v109
	v_cvt_pk_bf16_f32 v109, v162, v163
	v_mfma_f32_16x16x32_bf16 v[98:101], v[42:45], v[122:125], v[98:101]
	v_mfma_f32_16x16x32_bf16 v[126:129], v[122:125], v[122:125], v[126:129]
	v_mfma_f32_16x16x32_bf16 v[110:113], v[122:125], v[106:109], v[110:113]
	v_mfma_f32_16x16x32_bf16 v[102:105], v[10:13], v[122:125], v[102:105]
	v_mfma_f32_16x16x32_bf16 v[122:125], v[46:49], v[122:125], v[98:101]
	s_nop 5
	v_fma_f32 v110, v110, 2.0, v126
	v_fma_f32 v111, v111, 2.0, v127
	v_or_b32_e32 v126, 0xc0, v199
	v_cndmask_b32_e64 v127, v196, v126, s[6:7]
	v_mfma_f32_16x16x32_bf16 v[98:101], v[2:5], v[106:109], v[102:105]
	v_fma_f32 v112, v112, 2.0, v128
	v_fma_f32 v113, v113, 2.0, v129
	s_nop 0
	v_lshl_or_b32 v102, v127, 2, v198
	ds_write_b32 v102, v110
	v_cndmask_b32_e64 v110, v196, v126, s[4:5]
	v_mfma_f32_16x16x32_bf16 v[102:105], v[42:45], v[106:109], v[122:125]
	v_lshl_or_b32 v106, v110, 2, v198
	ds_write_b32 v106, v111
	v_cndmask_b32_e64 v106, v196, v126, s[2:3]
	v_lshl_or_b32 v106, v106, 2, v198
	ds_write_b32 v106, v112
	v_cndmask_b32_e32 v106, v196, v126, vcc
	v_lshl_or_b32 v106, v106, 2, v198
	ds_write_b32 v106, v113
	ds_read_b128 v[106:109], v197
	ds_read_b128 v[110:113], v197 offset:64
	ds_read_b128 v[202:205], v197 offset:128
	ds_read_b128 v[206:209], v197 offset:192
	s_mov_b32 s18, 0xdac100
	s_mov_b32 s19, 0xe29100
	buffer_load_dwordx4 v[122:125], v201, s[8:11], s18 offen nt
	buffer_load_dwordx4 v[126:129], v201, s[8:11], s19 offen nt
	s_mov_b32 s18, 0xea6100
	s_mov_b32 s19, 0xf23100
	buffer_load_dwordx4 v[162:165], v201, s[8:11], s18 offen nt
	buffer_load_dwordx4 v[166:169], v201, s[8:11], s19 offen nt
	s_waitcnt vmcnt(19)
	ds_write_b128 v200, v[130:133] offset:4608
	s_waitcnt vmcnt(18)
	ds_write_b128 v200, v[134:137] offset:5760
	s_waitcnt vmcnt(17)
	ds_write_b128 v200, v[170:173] offset:6912
	s_waitcnt vmcnt(16)
	ds_write_b128 v200, v[174:177] offset:8064
	s_waitcnt lgkmcnt(7)
	v_cvt_pk_bf16_f32 v130, v106, v107
	v_cvt_pk_bf16_f32 v131, v108, v109
	s_waitcnt lgkmcnt(6)
	v_cvt_pk_bf16_f32 v132, v110, v111
	v_cvt_pk_bf16_f32 v133, v112, v113
	v_lshlrev_b32_e32 v170, 16, v130
	v_and_b32_e32 v171, 0xffff0000, v130
	v_mfma_f32_16x16x32_bf16 v[134:137], v[22:25], v[130:133], 0
	v_add_f32_e64 v106, v106, -v170
	v_add_f32_e64 v107, v107, -v171
	v_lshlrev_b32_e32 v174, 16, v131
	v_and_b32_e32 v175, 0xffff0000, v131
	v_mfma_f32_16x16x32_bf16 v[170:173], v[34:37], v[130:133], 0
	v_add_f32_e64 v108, v108, -v174
	v_add_f32_e64 v109, v109, -v175
	v_cvt_pk_bf16_f32 v106, v106, v107
	v_cvt_pk_bf16_f32 v107, v108, v109
	v_lshlrev_b32_e32 v108, 16, v132
	v_and_b32_e32 v109, 0xffff0000, v132
	v_mfma_f32_16x16x32_bf16 v[134:137], v[30:33], v[130:133], v[134:137]
	v_add_f32_e64 v108, v110, -v108
	v_add_f32_e64 v109, v111, -v109
	v_lshlrev_b32_e32 v110, 16, v133
	v_and_b32_e32 v111, 0xffff0000, v133
	v_mfma_f32_16x16x32_bf16 v[170:173], v[38:41], v[130:133], v[170:173]
	v_add_f32_e64 v110, v112, -v110
	v_add_f32_e64 v111, v113, -v111
	v_cvt_pk_bf16_f32 v108, v108, v109
	v_cvt_pk_bf16_f32 v109, v110, v111
	v_mfma_f32_16x16x32_bf16 v[174:177], v[130:133], v[130:133], 0
	s_nop 0
	v_mfma_f32_16x16x32_bf16 v[110:113], v[130:133], v[106:109], 0
	v_mfma_f32_16x16x32_bf16 v[130:133], v[22:25], v[106:109], v[134:137]
	s_waitcnt lgkmcnt(5)
	s_nop 1
	v_cvt_pk_bf16_f32 v134, v202, v203
	v_lshlrev_b32_e32 v136, 16, v134
	v_and_b32_e32 v137, 0xffff0000, v134
	v_mfma_f32_16x16x32_bf16 v[106:109], v[34:37], v[106:109], v[170:173]
	v_add_f32_e64 v136, v202, -v136
	v_add_f32_e64 v137, v203, -v137
	v_cvt_pk_bf16_f32 v135, v204, v205
	v_cvt_pk_bf16_f32 v170, v136, v137
	s_waitcnt lgkmcnt(4)
	v_cvt_pk_bf16_f32 v136, v206, v207
	v_cvt_pk_bf16_f32 v137, v208, v209
	v_lshlrev_b32_e32 v172, 16, v135
	v_and_b32_e32 v173, 0xffff0000, v135
	v_mfma_f32_16x16x32_bf16 v[130:133], v[18:21], v[134:137], v[130:133]
	v_add_f32_e64 v172, v204, -v172
	v_add_f32_e64 v173, v205, -v173
	v_lshlrev_b32_e32 v202, 16, v137
	v_cvt_pk_bf16_f32 v171, v172, v173
	v_lshlrev_b32_e32 v172, 16, v136
	v_and_b32_e32 v173, 0xffff0000, v136
	v_and_b32_e32 v203, 0xffff0000, v137
	v_mfma_f32_16x16x32_bf16 v[106:109], v[66:69], v[134:137], v[106:109]
	v_add_f32_e64 v172, v206, -v172
	v_add_f32_e64 v173, v207, -v173
	v_pk_add_f32 v[202:203], v[208:209], v[202:203] neg_lo:[0,1] neg_hi:[0,1]
	v_cvt_pk_bf16_f32 v172, v172, v173
	v_cvt_pk_bf16_f32 v173, v202, v203
	v_mfma_f32_16x16x32_bf16 v[174:177], v[134:137], v[134:137], v[174:177]
	v_mfma_f32_16x16x32_bf16 v[130:133], v[26:29], v[134:137], v[130:133]
	v_mfma_f32_16x16x32_bf16 v[110:113], v[134:137], v[170:173], v[110:113]
	v_mfma_f32_16x16x32_bf16 v[106:109], v[70:73], v[134:137], v[106:109]
	v_or_b32_e32 v136, 0x50, v199
	v_cndmask_b32_e64 v137, v196, v136, s[6:7]
	s_nop 4
	v_pk_fma_f32 v[176:177], v[112:113], 2.0, v[176:177] op_sel_hi:[1,0,1]
	v_pk_fma_f32 v[134:135], v[110:111], 2.0, v[174:175] op_sel_hi:[1,0,1]
	v_mfma_f32_16x16x32_bf16 v[110:113], v[18:21], v[170:173], v[130:133]
	s_nop 2
	v_lshl_or_b32 v130, v137, 2, v198
	ds_write_b32 v130, v134
	v_cndmask_b32_e64 v130, v196, v136, s[4:5]
	v_lshl_or_b32 v130, v130, 2, v198
	v_mfma_f32_16x16x32_bf16 v[106:109], v[66:69], v[170:173], v[106:109]
	ds_write_b32 v130, v135
	v_cndmask_b32_e64 v130, v196, v136, s[2:3]
	v_lshl_or_b32 v130, v130, 2, v198
	ds_write_b32 v130, v176
	v_cndmask_b32_e32 v130, v196, v136, vcc
	v_lshl_or_b32 v130, v130, 2, v198
	ds_write_b32 v130, v177
	ds_read_b128 v[130:133], v197 offset:4608
	ds_read_b128 v[134:137], v197 offset:4672
	ds_read_b128 v[170:173], v197 offset:4736
	ds_read_b128 v[174:177], v197 offset:4800
	s_waitcnt vmcnt(15)
	ds_write_b128 v200, v[138:141]
	s_waitcnt vmcnt(14)
	ds_write_b128 v200, v[142:145] offset:1152
	s_waitcnt vmcnt(13)
	ds_write_b128 v200, v[178:181] offset:2304
	s_waitcnt vmcnt(12)
	ds_write_b128 v200, v[182:185] offset:3456
	s_waitcnt lgkmcnt(7)
	v_cvt_pk_bf16_f32 v138, v130, v131
	v_cvt_pk_bf16_f32 v139, v132, v133
	s_waitcnt lgkmcnt(6)
	v_cvt_pk_bf16_f32 v140, v134, v135
	v_cvt_pk_bf16_f32 v141, v136, v137
	v_lshlrev_b32_e32 v142, 16, v138
	v_and_b32_e32 v143, 0xffff0000, v138
	v_mfma_f32_16x16x32_bf16 v[110:113], v[6:9], v[138:141], v[110:113]
	v_add_f32_e64 v130, v130, -v142
	v_add_f32_e64 v131, v131, -v143
	v_lshlrev_b32_e32 v142, 16, v139
	v_and_b32_e32 v143, 0xffff0000, v139
	v_mfma_f32_16x16x32_bf16 v[106:109], v[50:53], v[138:141], v[106:109]
	v_add_f32_e64 v132, v132, -v142
	v_add_f32_e64 v133, v133, -v143
	v_cvt_pk_bf16_f32 v130, v130, v131
	v_cvt_pk_bf16_f32 v131, v132, v133
	v_lshlrev_b32_e32 v132, 16, v140
	v_and_b32_e32 v133, 0xffff0000, v140
	v_mfma_f32_16x16x32_bf16 v[110:113], v[14:17], v[138:141], v[110:113]
	v_add_f32_e64 v132, v134, -v132
	v_add_f32_e64 v133, v135, -v133
	v_lshlrev_b32_e32 v134, 16, v141
	v_and_b32_e32 v135, 0xffff0000, v141
	v_mfma_f32_16x16x32_bf16 v[106:109], v[54:57], v[138:141], v[106:109]
	v_add_f32_e64 v134, v136, -v134
	v_add_f32_e64 v135, v137, -v135
	v_cvt_pk_bf16_f32 v132, v132, v133
	v_cvt_pk_bf16_f32 v133, v134, v135
	v_mfma_f32_16x16x32_bf16 v[142:145], v[138:141], v[138:141], 0
	s_nop 0
	v_mfma_f32_16x16x32_bf16 v[134:137], v[138:141], v[130:133], 0
	s_waitcnt lgkmcnt(5)
	v_cvt_pk_bf16_f32 v138, v170, v171
	v_lshlrev_b32_e32 v140, 16, v138
	v_and_b32_e32 v141, 0xffff0000, v138
	v_mfma_f32_16x16x32_bf16 v[110:113], v[6:9], v[130:133], v[110:113]
	v_cvt_pk_bf16_f32 v139, v172, v173
	v_mfma_f32_16x16x32_bf16 v[106:109], v[50:53], v[130:133], v[106:109]
	v_add_f32_e64 v130, v170, -v140
	v_add_f32_e64 v131, v171, -v141
	s_waitcnt lgkmcnt(4)
	v_cvt_pk_bf16_f32 v140, v174, v175
	v_cvt_pk_bf16_f32 v141, v176, v177
	v_lshlrev_b32_e32 v132, 16, v139
	v_and_b32_e32 v133, 0xffff0000, v139
	v_pk_add_f32 v[132:133], v[172:173], v[132:133] neg_lo:[0,1] neg_hi:[0,1]
	v_cvt_pk_bf16_f32 v130, v130, v131
	v_cvt_pk_bf16_f32 v131, v132, v133
	v_lshlrev_b32_e32 v132, 16, v140
	v_and_b32_e32 v133, 0xffff0000, v140
	v_lshlrev_b32_e32 v170, 16, v141
	v_and_b32_e32 v171, 0xffff0000, v141
	v_mfma_f32_16x16x32_bf16 v[110:113], v[2:5], v[138:141], v[110:113]
	v_add_f32_e64 v132, v174, -v132
	v_add_f32_e64 v133, v175, -v133
	v_pk_add_f32 v[170:171], v[176:177], v[170:171] neg_lo:[0,1] neg_hi:[0,1]
	v_cvt_pk_bf16_f32 v132, v132, v133
	v_cvt_pk_bf16_f32 v133, v170, v171
	v_mfma_f32_16x16x32_bf16 v[106:109], v[42:45], v[138:141], v[106:109]
	v_mfma_f32_16x16x32_bf16 v[142:145], v[138:141], v[138:141], v[142:145]
	v_mfma_f32_16x16x32_bf16 v[134:137], v[138:141], v[130:133], v[134:137]
	v_mfma_f32_16x16x32_bf16 v[110:113], v[10:13], v[138:141], v[110:113]
	s_nop 6
	v_fma_f32 v144, v136, 2.0, v144
	v_fma_f32 v145, v137, 2.0, v145
	v_mfma_f32_16x16x32_bf16 v[136:139], v[46:49], v[138:141], v[106:109]
	v_or_b32_e32 v140, 0xd0, v199
	v_cndmask_b32_e64 v141, v196, v140, s[6:7]
	v_pk_fma_f32 v[134:135], v[134:135], 2.0, v[142:143] op_sel_hi:[1,0,1]
	v_mfma_f32_16x16x32_bf16 v[106:109], v[2:5], v[130:133], v[110:113]
	s_nop 2
	v_lshl_or_b32 v110, v141, 2, v198
	ds_write_b32 v110, v134
	v_cndmask_b32_e64 v134, v196, v140, s[4:5]
	v_mfma_f32_16x16x32_bf16 v[110:113], v[42:45], v[130:133], v[136:139]
	v_lshl_or_b32 v130, v134, 2, v198
	ds_write_b32 v130, v135
	v_cndmask_b32_e64 v130, v196, v140, s[2:3]
	v_lshl_or_b32 v130, v130, 2, v198
	ds_write_b32 v130, v144
	v_cndmask_b32_e32 v130, v196, v140, vcc
	v_lshl_or_b32 v130, v130, 2, v198
	ds_write_b32 v130, v145
	ds_read_b128 v[130:133], v197
	ds_read_b128 v[134:137], v197 offset:64
	ds_read_b128 v[138:141], v197 offset:128
	ds_read_b128 v[142:145], v197 offset:192
	s_waitcnt vmcnt(11)
	ds_write_b128 v200, v[146:149] offset:4608
	s_waitcnt vmcnt(10)
	ds_write_b128 v200, v[150:153] offset:5760
	s_waitcnt vmcnt(9)
	ds_write_b128 v200, v[186:189] offset:6912
	s_waitcnt vmcnt(8)
	ds_write_b128 v200, v[190:193] offset:8064
	s_waitcnt lgkmcnt(7)
	v_cvt_pk_bf16_f32 v146, v130, v131
	v_cvt_pk_bf16_f32 v147, v132, v133
	s_waitcnt lgkmcnt(6)
	v_cvt_pk_bf16_f32 v148, v134, v135
	v_cvt_pk_bf16_f32 v149, v136, v137
	v_lshlrev_b32_e32 v170, 16, v146
	v_and_b32_e32 v171, 0xffff0000, v146
	v_mfma_f32_16x16x32_bf16 v[150:153], v[22:25], v[146:149], 0
	v_add_f32_e64 v130, v130, -v170
	v_add_f32_e64 v131, v131, -v171
	v_lshlrev_b32_e32 v174, 16, v147
	v_and_b32_e32 v175, 0xffff0000, v147
	v_mfma_f32_16x16x32_bf16 v[170:173], v[34:37], v[146:149], 0
	v_add_f32_e64 v132, v132, -v174
	v_add_f32_e64 v133, v133, -v175
	v_cvt_pk_bf16_f32 v130, v130, v131
	v_cvt_pk_bf16_f32 v131, v132, v133
	v_lshlrev_b32_e32 v132, 16, v148
	v_and_b32_e32 v133, 0xffff0000, v148
	v_mfma_f32_16x16x32_bf16 v[150:153], v[30:33], v[146:149], v[150:153]
	v_add_f32_e64 v132, v134, -v132
	v_add_f32_e64 v133, v135, -v133
	v_lshlrev_b32_e32 v134, 16, v149
	v_and_b32_e32 v135, 0xffff0000, v149
	v_mfma_f32_16x16x32_bf16 v[170:173], v[38:41], v[146:149], v[170:173]
	v_add_f32_e64 v134, v136, -v134
	v_add_f32_e64 v135, v137, -v135
	v_cvt_pk_bf16_f32 v132, v132, v133
	v_cvt_pk_bf16_f32 v133, v134, v135
	v_mfma_f32_16x16x32_bf16 v[174:177], v[146:149], v[146:149], 0
	s_nop 0
	v_mfma_f32_16x16x32_bf16 v[134:137], v[146:149], v[130:133], 0
	v_mfma_f32_16x16x32_bf16 v[146:149], v[22:25], v[130:133], v[150:153]
	s_waitcnt lgkmcnt(5)
	s_nop 1
	v_cvt_pk_bf16_f32 v150, v138, v139
	v_cvt_pk_bf16_f32 v151, v140, v141
	v_lshlrev_b32_e32 v152, 16, v150
	v_and_b32_e32 v153, 0xffff0000, v150
	v_mfma_f32_16x16x32_bf16 v[130:133], v[34:37], v[130:133], v[170:173]
	v_add_f32_e64 v138, v138, -v152
	v_add_f32_e64 v139, v139, -v153
	s_waitcnt lgkmcnt(4)
	v_cvt_pk_bf16_f32 v152, v142, v143
	v_cvt_pk_bf16_f32 v153, v144, v145
	v_lshlrev_b32_e32 v170, 16, v151
	v_and_b32_e32 v171, 0xffff0000, v151
	v_pk_add_f32 v[140:141], v[140:141], v[170:171] neg_lo:[0,1] neg_hi:[0,1]
	v_cvt_pk_bf16_f32 v138, v138, v139
	v_mfma_f32_16x16x32_bf16 v[146:149], v[18:21], v[150:153], v[146:149]
	v_cvt_pk_bf16_f32 v139, v140, v141
	v_lshlrev_b32_e32 v140, 16, v152
	v_and_b32_e32 v141, 0xffff0000, v152
	v_pk_add_f32 v[140:141], v[142:143], v[140:141] neg_lo:[0,1] neg_hi:[0,1]
	v_lshlrev_b32_e32 v142, 16, v153
	v_and_b32_e32 v143, 0xffff0000, v153
	v_mfma_f32_16x16x32_bf16 v[130:133], v[66:69], v[150:153], v[130:133]
	v_add_f32_e64 v142, v144, -v142
	v_add_f32_e64 v143, v145, -v143
	v_cvt_pk_bf16_f32 v140, v140, v141
	v_cvt_pk_bf16_f32 v141, v142, v143
	v_mfma_f32_16x16x32_bf16 v[170:173], v[150:153], v[150:153], v[174:177]
	v_mfma_f32_16x16x32_bf16 v[146:149], v[26:29], v[150:153], v[146:149]
	v_mfma_f32_16x16x32_bf16 v[134:137], v[150:153], v[138:141], v[134:137]
	v_mfma_f32_16x16x32_bf16 v[130:133], v[70:73], v[150:153], v[130:133]
	v_or_b32_e32 v150, 0x60, v199
	v_cndmask_b32_e64 v151, v196, v150, s[6:7]
	s_nop 4
	v_pk_fma_f32 v[142:143], v[136:137], 2.0, v[172:173] op_sel_hi:[1,0,1]
	v_pk_fma_f32 v[144:145], v[134:135], 2.0, v[170:171] op_sel_hi:[1,0,1]
	v_mfma_f32_16x16x32_bf16 v[134:137], v[18:21], v[138:141], v[146:149]
	s_nop 2
	v_lshl_or_b32 v146, v151, 2, v198
	ds_write_b32 v146, v144
	v_cndmask_b32_e64 v144, v196, v150, s[4:5]
	v_mfma_f32_16x16x32_bf16 v[130:133], v[66:69], v[138:141], v[130:133]
	v_lshl_or_b32 v138, v144, 2, v198
	ds_write_b32 v138, v145
	v_cndmask_b32_e64 v138, v196, v150, s[2:3]
	v_lshl_or_b32 v138, v138, 2, v198
	ds_write_b32 v138, v142
	v_cndmask_b32_e32 v138, v196, v150, vcc
	v_lshl_or_b32 v138, v138, 2, v198
	ds_write_b32 v138, v143
	ds_read_b128 v[138:141], v197 offset:4608
	ds_read_b128 v[142:145], v197 offset:4672
	ds_read_b128 v[146:149], v197 offset:4736
	ds_read_b128 v[150:153], v197 offset:4800
	s_waitcnt vmcnt(7)
	ds_write_b128 v200, v[114:117]
	s_waitcnt vmcnt(6)
	ds_write_b128 v200, v[118:121] offset:1152
	s_waitcnt vmcnt(5)
	ds_write_b128 v200, v[154:157] offset:2304
	s_waitcnt vmcnt(4)
	ds_write_b128 v200, v[158:161] offset:3456
	s_waitcnt lgkmcnt(7)
	v_cvt_pk_bf16_f32 v114, v138, v139
	v_cvt_pk_bf16_f32 v115, v140, v141
	s_waitcnt lgkmcnt(6)
	v_cvt_pk_bf16_f32 v116, v142, v143
	v_cvt_pk_bf16_f32 v117, v144, v145
	v_lshlrev_b32_e32 v154, 16, v114
	v_and_b32_e32 v155, 0xffff0000, v114
	v_mfma_f32_16x16x32_bf16 v[118:121], v[6:9], v[114:117], v[134:137]
	v_mfma_f32_16x16x32_bf16 v[130:133], v[50:53], v[114:117], v[130:133]
	s_nop 1
	v_lshlrev_b32_e32 v136, 16, v115
	v_and_b32_e32 v137, 0xffff0000, v115
	v_pk_add_f32 v[134:135], v[138:139], v[154:155] neg_lo:[0,1] neg_hi:[0,1]
	v_pk_add_f32 v[136:137], v[140:141], v[136:137] neg_lo:[0,1] neg_hi:[0,1]
	v_cvt_pk_bf16_f32 v134, v134, v135
	v_cvt_pk_bf16_f32 v135, v136, v137
	v_lshlrev_b32_e32 v136, 16, v116
	v_and_b32_e32 v137, 0xffff0000, v116
	v_mfma_f32_16x16x32_bf16 v[118:121], v[14:17], v[114:117], v[118:121]
	v_add_f32_e64 v136, v142, -v136
	v_add_f32_e64 v137, v143, -v137
	v_lshlrev_b32_e32 v142, 16, v117
	v_and_b32_e32 v143, 0xffff0000, v117
	v_mfma_f32_16x16x32_bf16 v[130:133], v[54:57], v[114:117], v[130:133]
	v_add_f32_e64 v142, v144, -v142
	v_add_f32_e64 v143, v145, -v143
	v_cvt_pk_bf16_f32 v136, v136, v137
	v_cvt_pk_bf16_f32 v137, v142, v143
	s_waitcnt lgkmcnt(5)
	v_cvt_pk_bf16_f32 v142, v146, v147
	v_lshlrev_b32_e32 v144, 16, v142
	v_mfma_f32_16x16x32_bf16 v[118:121], v[6:9], v[134:137], v[118:121]
	v_and_b32_e32 v145, 0xffff0000, v142
	v_cvt_pk_bf16_f32 v143, v148, v149
	v_mfma_f32_16x16x32_bf16 v[130:133], v[50:53], v[134:137], v[130:133]
	v_mfma_f32_16x16x32_bf16 v[138:141], v[114:117], v[114:117], 0
	v_mfma_f32_16x16x32_bf16 v[114:117], v[114:117], v[134:137], 0
	v_add_f32_e64 v134, v146, -v144
	v_add_f32_e64 v135, v147, -v145
	s_waitcnt lgkmcnt(4)
	v_cvt_pk_bf16_f32 v144, v150, v151
	v_cvt_pk_bf16_f32 v145, v152, v153
	v_lshlrev_b32_e32 v136, 16, v143
	v_and_b32_e32 v137, 0xffff0000, v143
	v_mfma_f32_16x16x32_bf16 v[118:121], v[2:5], v[142:145], v[118:121]
	v_add_f32_e64 v136, v148, -v136
	v_add_f32_e64 v137, v149, -v137
	v_cvt_pk_bf16_f32 v134, v134, v135
	v_cvt_pk_bf16_f32 v135, v136, v137
	v_lshlrev_b32_e32 v136, 16, v144
	v_and_b32_e32 v137, 0xffff0000, v144
	v_lshlrev_b32_e32 v146, 16, v145
	v_and_b32_e32 v147, 0xffff0000, v145
	v_mfma_f32_16x16x32_bf16 v[130:133], v[42:45], v[142:145], v[130:133]
	v_add_f32_e64 v136, v150, -v136
	v_add_f32_e64 v137, v151, -v137
	v_pk_add_f32 v[146:147], v[152:153], v[146:147] neg_lo:[0,1] neg_hi:[0,1]
	v_cvt_pk_bf16_f32 v136, v136, v137
	v_cvt_pk_bf16_f32 v137, v146, v147
	v_mfma_f32_16x16x32_bf16 v[138:141], v[142:145], v[142:145], v[138:141]
	v_mfma_f32_16x16x32_bf16 v[118:121], v[10:13], v[142:145], v[118:121]
	v_mfma_f32_16x16x32_bf16 v[114:117], v[142:145], v[134:137], v[114:117]
	v_mfma_f32_16x16x32_bf16 v[130:133], v[46:49], v[142:145], v[130:133]
	v_or_b32_e32 v142, 0xe0, v199
	v_cndmask_b32_e64 v143, v196, v142, s[6:7]
	s_nop 4
	v_pk_fma_f32 v[140:141], v[116:117], 2.0, v[140:141] op_sel_hi:[1,0,1]
	v_pk_fma_f32 v[138:139], v[114:115], 2.0, v[138:139] op_sel_hi:[1,0,1]
	v_mfma_f32_16x16x32_bf16 v[114:117], v[2:5], v[134:137], v[118:121]
	s_nop 2
	v_lshl_or_b32 v118, v143, 2, v198
	ds_write_b32 v118, v138
	v_cndmask_b32_e64 v138, v196, v142, s[4:5]
	v_mfma_f32_16x16x32_bf16 v[118:121], v[42:45], v[134:137], v[130:133]
	s_nop 2
	v_lshl_or_b32 v130, v138, 2, v198
	ds_write_b32 v130, v139
	v_cndmask_b32_e64 v130, v196, v142, s[2:3]
	v_lshl_or_b32 v130, v130, 2, v198
	ds_write_b32 v130, v140
	v_cndmask_b32_e32 v130, v196, v142, vcc
	v_lshl_or_b32 v130, v130, 2, v198
	ds_write_b32 v130, v141
	ds_read_b128 v[130:133], v197
	ds_read_b128 v[134:137], v197 offset:64
	ds_read_b128 v[138:141], v197 offset:128
	ds_read_b128 v[142:145], v197 offset:192
	s_waitcnt vmcnt(3)
	ds_write_b128 v200, v[122:125] offset:4608
	s_waitcnt vmcnt(2)
	ds_write_b128 v200, v[126:129] offset:5760
	s_waitcnt vmcnt(1)
	ds_write_b128 v200, v[162:165] offset:6912
	s_waitcnt vmcnt(0)
	ds_write_b128 v200, v[166:169] offset:8064
	s_waitcnt lgkmcnt(7)
	v_cvt_pk_bf16_f32 v122, v130, v131
	v_cvt_pk_bf16_f32 v123, v132, v133
	s_waitcnt lgkmcnt(6)
	v_cvt_pk_bf16_f32 v124, v134, v135
	v_cvt_pk_bf16_f32 v125, v136, v137
	v_lshlrev_b32_e32 v146, 16, v122
	v_and_b32_e32 v147, 0xffff0000, v122
	v_mfma_f32_16x16x32_bf16 v[126:129], v[22:25], v[122:125], 0
	v_lshlrev_b32_e32 v150, 16, v123
	v_and_b32_e32 v151, 0xffff0000, v123
	v_pk_add_f32 v[130:131], v[130:131], v[146:147] neg_lo:[0,1] neg_hi:[0,1]
	v_pk_add_f32 v[132:133], v[132:133], v[150:151] neg_lo:[0,1] neg_hi:[0,1]
	v_cvt_pk_bf16_f32 v130, v130, v131
	v_mfma_f32_16x16x32_bf16 v[146:149], v[34:37], v[122:125], 0
	v_cvt_pk_bf16_f32 v131, v132, v133
	v_lshlrev_b32_e32 v132, 16, v124
	v_and_b32_e32 v133, 0xffff0000, v124
	v_mfma_f32_16x16x32_bf16 v[30:33], v[30:33], v[122:125], v[126:129]
	s_nop 2
	v_add_f32_e64 v126, v134, -v132
	v_add_f32_e64 v127, v135, -v133
	v_mfma_f32_16x16x32_bf16 v[38:41], v[38:41], v[122:125], v[146:149]
	v_cvt_pk_bf16_f32 v132, v126, v127
	v_lshlrev_b32_e32 v126, 16, v125
	v_and_b32_e32 v127, 0xffff0000, v125
	v_pk_add_f32 v[126:127], v[136:137], v[126:127] neg_lo:[0,1] neg_hi:[0,1]
	v_mfma_f32_16x16x32_bf16 v[150:153], v[122:125], v[122:125], 0
	v_cvt_pk_bf16_f32 v133, v126, v127
	s_nop 1
	v_mfma_f32_16x16x32_bf16 v[22:25], v[22:25], v[130:133], v[30:33]
	s_waitcnt lgkmcnt(5)
	s_nop 1
	v_cvt_pk_bf16_f32 v30, v138, v139
	v_lshlrev_b32_e32 v32, 16, v30
	v_and_b32_e32 v33, 0xffff0000, v30
	v_pk_add_f32 v[32:33], v[138:139], v[32:33] neg_lo:[0,1] neg_hi:[0,1]
	v_mfma_f32_16x16x32_bf16 v[34:37], v[34:37], v[130:133], v[38:41]
	v_cvt_pk_bf16_f32 v31, v140, v141
	s_nop 1
	v_cvt_pk_bf16_f32 v38, v32, v33
	s_waitcnt lgkmcnt(4)
	v_cvt_pk_bf16_f32 v32, v142, v143
	v_cvt_pk_bf16_f32 v33, v144, v145
	v_lshlrev_b32_e32 v40, 16, v31
	v_and_b32_e32 v41, 0xffff0000, v31
	v_mfma_f32_16x16x32_bf16 v[22:25], v[18:21], v[30:33], v[22:25]
	v_add_f32_e64 v40, v140, -v40
	v_add_f32_e64 v41, v141, -v41
	v_cvt_pk_bf16_f32 v39, v40, v41
	v_mfma_f32_16x16x32_bf16 v[122:125], v[122:125], v[130:133], 0
	v_lshlrev_b32_e32 v40, 16, v32
	v_and_b32_e32 v41, 0xffff0000, v32
	v_lshlrev_b32_e32 v130, 16, v33
	v_and_b32_e32 v131, 0xffff0000, v33
	v_pk_add_f32 v[40:41], v[142:143], v[40:41] neg_lo:[0,1] neg_hi:[0,1]
	v_mfma_f32_16x16x32_bf16 v[22:25], v[26:29], v[30:33], v[22:25]
	v_add_f32_e64 v26, v144, -v130
	v_add_f32_e64 v27, v145, -v131
	v_cvt_pk_bf16_f32 v40, v40, v41
	v_cvt_pk_bf16_f32 v41, v26, v27
	v_mfma_f32_16x16x32_bf16 v[34:37], v[66:69], v[30:33], v[34:37]
	v_mfma_f32_16x16x32_bf16 v[126:129], v[30:33], v[30:33], v[150:153]
	v_mfma_f32_16x16x32_bf16 v[26:29], v[30:33], v[38:41], v[122:125]
	v_mfma_f32_16x16x32_bf16 v[18:21], v[18:21], v[38:41], v[22:25]
	s_nop 6
	v_fma_f32 v122, v28, 2.0, v128
	v_fma_f32 v123, v29, 2.0, v129
	v_mfma_f32_16x16x32_bf16 v[28:31], v[70:73], v[30:33], v[34:37]
	v_or_b32_e32 v32, 0x70, v199
	v_cndmask_b32_e64 v33, v196, v32, s[6:7]
	v_pk_fma_f32 v[26:27], v[26:27], 2.0, v[126:127] op_sel_hi:[1,0,1]
	v_lshl_or_b32 v22, v33, 2, v198
	ds_write_b32 v22, v26
	v_cndmask_b32_e64 v26, v196, v32, s[4:5]
	v_lshl_or_b32 v26, v26, 2, v198
	ds_write_b32 v26, v27
	v_cndmask_b32_e64 v26, v196, v32, s[2:3]
	v_lshl_or_b32 v26, v26, 2, v198
	ds_write_b32 v26, v122
	v_cndmask_b32_e32 v26, v196, v32, vcc
	v_lshl_or_b32 v26, v26, 2, v198
	v_mfma_f32_16x16x32_bf16 v[22:25], v[66:69], v[38:41], v[28:31]
	ds_write_b32 v26, v123
	s_nop 1
	ds_read_b128 v[26:29], v197 offset:4608
	ds_read_b128 v[30:33], v197 offset:4672
	ds_read_b128 v[34:37], v197 offset:4736
	ds_read_b128 v[38:41], v197 offset:4800
	s_waitcnt lgkmcnt(3)
	v_cvt_pk_bf16_f32 v66, v26, v27
	v_cvt_pk_bf16_f32 v67, v28, v29
	s_waitcnt lgkmcnt(2)
	v_cvt_pk_bf16_f32 v68, v30, v31
	v_cvt_pk_bf16_f32 v69, v32, v33
	v_lshlrev_b32_e32 v70, 16, v66
	v_and_b32_e32 v71, 0xffff0000, v66
	v_mfma_f32_16x16x32_bf16 v[18:21], v[6:9], v[66:69], v[18:21]
	v_add_f32_e64 v26, v26, -v70
	v_add_f32_e64 v27, v27, -v71
	v_lshlrev_b32_e32 v70, 16, v67
	v_and_b32_e32 v71, 0xffff0000, v67
	v_mfma_f32_16x16x32_bf16 v[22:25], v[50:53], v[66:69], v[22:25]
	v_add_f32_e64 v28, v28, -v70
	v_add_f32_e64 v29, v29, -v71
	v_cvt_pk_bf16_f32 v26, v26, v27
	v_cvt_pk_bf16_f32 v27, v28, v29
	v_lshlrev_b32_e32 v28, 16, v68
	v_and_b32_e32 v29, 0xffff0000, v68
	v_mfma_f32_16x16x32_bf16 v[14:17], v[14:17], v[66:69], v[18:21]
	s_nop 2
	v_add_f32_e64 v18, v30, -v28
	v_add_f32_e64 v19, v31, -v29
	v_lshlrev_b32_e32 v30, 16, v69
	v_and_b32_e32 v31, 0xffff0000, v69
	v_cvt_pk_bf16_f32 v28, v18, v19
	v_mfma_f32_16x16x32_bf16 v[18:21], v[54:57], v[66:69], v[22:25]
	s_nop 2
	v_add_f32_e64 v22, v32, -v30
	v_add_f32_e64 v23, v33, -v31
	v_mfma_f32_16x16x32_bf16 v[70:73], v[66:69], v[66:69], 0
	v_cvt_pk_bf16_f32 v29, v22, v23
	s_nop 1
	v_mfma_f32_16x16x32_bf16 v[6:9], v[6:9], v[26:29], v[14:17]
	s_waitcnt lgkmcnt(1)
	s_nop 1
	v_cvt_pk_bf16_f32 v14, v34, v35
	v_lshlrev_b32_e32 v16, 16, v14
	v_and_b32_e32 v17, 0xffff0000, v14
	v_pk_add_f32 v[16:17], v[34:35], v[16:17] neg_lo:[0,1] neg_hi:[0,1]
	v_mfma_f32_16x16x32_bf16 v[22:25], v[66:69], v[26:29], 0
	v_cvt_pk_bf16_f32 v15, v36, v37
	v_mfma_f32_16x16x32_bf16 v[18:21], v[50:53], v[26:29], v[18:21]
	v_cvt_pk_bf16_f32 v26, v16, v17
	s_waitcnt lgkmcnt(0)
	v_cvt_pk_bf16_f32 v16, v38, v39
	v_cvt_pk_bf16_f32 v17, v40, v41
	v_lshlrev_b32_e32 v28, 16, v15
	v_and_b32_e32 v29, 0xffff0000, v15
	v_mfma_f32_16x16x32_bf16 v[6:9], v[2:5], v[14:17], v[6:9]
	v_add_f32_e64 v28, v36, -v28
	v_add_f32_e64 v29, v37, -v29
	v_lshlrev_b32_e32 v34, 16, v17
	v_cvt_pk_bf16_f32 v27, v28, v29
	v_lshlrev_b32_e32 v28, 16, v16
	v_and_b32_e32 v29, 0xffff0000, v16
	v_and_b32_e32 v35, 0xffff0000, v17
	v_pk_add_f32 v[28:29], v[38:39], v[28:29] neg_lo:[0,1] neg_hi:[0,1]
	v_mfma_f32_16x16x32_bf16 v[6:9], v[10:13], v[14:17], v[6:9]
	v_add_f32_e64 v10, v40, -v34
	v_add_f32_e64 v11, v41, -v35
	v_cvt_pk_bf16_f32 v28, v28, v29
	v_cvt_pk_bf16_f32 v29, v10, v11
	v_mfma_f32_16x16x32_bf16 v[18:21], v[42:45], v[14:17], v[18:21]
	v_mfma_f32_16x16x32_bf16 v[30:33], v[14:17], v[14:17], v[70:73]
	v_mfma_f32_16x16x32_bf16 v[10:13], v[14:17], v[26:29], v[22:25]
	v_mfma_f32_16x16x32_bf16 v[2:5], v[2:5], v[26:29], v[6:9]
	s_nop 6
	v_fma_f32 v22, v12, 2.0, v32
	v_fma_f32 v23, v13, 2.0, v33
	v_mfma_f32_16x16x32_bf16 v[12:15], v[46:49], v[14:17], v[18:21]
	v_or_b32_e32 v16, 0xf0, v199
	v_cndmask_b32_e64 v17, v196, v16, s[6:7]
	v_pk_fma_f32 v[10:11], v[10:11], 2.0, v[30:31] op_sel_hi:[1,0,1]
	v_lshl_or_b32 v6, v17, 2, v198
	ds_write_b32 v6, v10
	v_cndmask_b32_e64 v10, v196, v16, s[4:5]
	v_lshl_or_b32 v10, v10, 2, v198
	v_mfma_f32_16x16x32_bf16 v[6:9], v[42:45], v[26:29], v[12:15]
	ds_write_b32 v10, v11
	v_cndmask_b32_e64 v10, v196, v16, s[2:3]
	v_lshl_or_b32 v10, v10, 2, v198
	ds_write_b32 v10, v22
	v_cndmask_b32_e32 v10, v196, v16, vcc
	v_lshl_or_b32 v10, v10, 2, v198
	ds_write_b32 v10, v23

	.amdhsa_kernel _Z9k1_streamPKfS0_PfS1_
		.amdhsa_group_segment_fixed_size 141312
		.amdhsa_private_segment_fixed_size 0
		.amdhsa_kernarg_size 32
		.amdhsa_user_sgpr_count 2
		.amdhsa_user_sgpr_dispatch_ptr 0
		.amdhsa_user_sgpr_queue_ptr 0
		.amdhsa_user_sgpr_kernarg_segment_ptr 1
		.amdhsa_user_sgpr_dispatch_id 0
		.amdhsa_user_sgpr_kernarg_preload_length 0
		.amdhsa_user_sgpr_kernarg_preload_offset 0
		.amdhsa_user_sgpr_private_segment_size 0
		.amdhsa_uses_dynamic_stack 0
		.amdhsa_enable_private_segment 0
		.amdhsa_system_sgpr_workgroup_id_x 1
		.amdhsa_system_sgpr_workgroup_id_y 0
		.amdhsa_system_sgpr_workgroup_id_z 0
		.amdhsa_system_sgpr_workgroup_info 0
		.amdhsa_system_vgpr_workitem_id 0
		.amdhsa_next_free_vgpr 256
		.amdhsa_next_free_sgpr 96
		.amdhsa_accum_offset 256
		.amdhsa_reserve_vcc 1
		.amdhsa_float_round_mode_32 0
		.amdhsa_float_round_mode_16_64 0
		.amdhsa_float_denorm_mode_32 3
		.amdhsa_float_denorm_mode_16_64 3
		.amdhsa_dx10_clamp 1
		.amdhsa_ieee_mode 1
		.amdhsa_fp16_overflow 0
		.amdhsa_tg_split 0
		.amdhsa_exception_fp_ieee_invalid_op 0
		.amdhsa_exception_fp_denorm_src 0
		.amdhsa_exception_fp_ieee_div_zero 0
		.amdhsa_exception_fp_ieee_overflow 0
		.amdhsa_exception_fp_ieee_underflow 0
		.amdhsa_exception_fp_ieee_inexact 0
		.amdhsa_exception_int_div_zero 0
	.end_amdhsa_kernel

amdhsa.kernels:
  - .agpr_count:     0
    .args:
      - .actual_access:  read_only
        .address_space:  global
        .offset:         0
        .size:           8
        .value_kind:     global_buffer
      - .actual_access:  read_only
        .address_space:  global
        .offset:         8
        .size:           8
        .value_kind:     global_buffer
      - .actual_access:  write_only
        .address_space:  global
        .offset:         16
        .size:           8
        .value_kind:     global_buffer
      - .actual_access:  write_only
        .address_space:  global
        .offset:         24
        .size:           8
        .value_kind:     global_buffer
    .group_segment_fixed_size: 141312
    .kernarg_segment_align: 8
    .kernarg_segment_size: 32
    .language:       OpenCL C
    .language_version:
      - 2
      - 0
    .max_flat_workgroup_size: 512
    .name:           _Z9k1_streamPKfS0_PfS1_
    .private_segment_fixed_size: 0
    .sgpr_count:     26
    .sgpr_spill_count: 0
    .symbol:         _Z9k1_streamPKfS0_PfS1_.kd
    .uniform_work_group_size: 1
    .uses_dynamic_stack: false
    .vgpr_count:     256
    .vgpr_spill_count: 0
    .wavefront_size: 64
  - .agpr_count:     0
    .args:
      - .actual_access:  read_only
        .address_space:  global
        .offset:         0
        .size:           8
        .value_kind:     global_buffer
      - .actual_access:  read_only
        .address_space:  global
        .offset:         8
        .size:           8
        .value_kind:     global_buffer
      - .actual_access:  read_only
        .address_space:  global
        .offset:         16
        .size:           8
        .value_kind:     global_buffer
      - .actual_access:  write_only
        .address_space:  global
        .offset:         24
        .size:           8
        .value_kind:     global_buffer
      - .actual_access:  write_only
        .address_space:  global
        .offset:         32
        .size:           8
        .value_kind:     global_buffer
      - .actual_access:  write_only
        .address_space:  global
        .offset:         40
        .size:           8
        .value_kind:     global_buffer
    .group_segment_fixed_size: 40
    .kernarg_segment_align: 8
    .kernarg_segment_size: 48
    .language:       OpenCL C
    .language_version:
      - 2
      - 0
    .max_flat_workgroup_size: 128
    .name:           _Z9k2_reducePKfS0_S0_PdPiS1_
    .private_segment_fixed_size: 0
    .sgpr_count:     40
    .sgpr_spill_count: 0
    .symbol:         _Z9k2_reducePKfS0_S0_PdPiS1_.kd
    .uniform_work_group_size: 1
    .uses_dynamic_stack: false
    .vgpr_count:     104
    .vgpr_spill_count: 0
    .wavefront_size: 64
  - .agpr_count:     0
    .args:
      - .actual_access:  read_only
        .address_space:  global
        .offset:         0
        .size:           8
        .value_kind:     global_buffer
      - .actual_access:  read_only
        .address_space:  global
        .offset:         8
        .size:           8
        .value_kind:     global_buffer
      - .actual_access:  read_only
        .address_space:  global
        .offset:         16
        .size:           8
        .value_kind:     global_buffer
      - .actual_access:  read_only
        .address_space:  global
        .offset:         24
        .size:           8
        .value_kind:     global_buffer
      - .actual_access:  read_only
        .address_space:  global
        .offset:         32
        .size:           8
        .value_kind:     global_buffer
      - .actual_access:  write_only
        .address_space:  global
        .offset:         40
        .size:           8
        .value_kind:     global_buffer
    .group_segment_fixed_size: 128
    .kernarg_segment_align: 8
    .kernarg_segment_size: 48
    .language:       OpenCL C
    .language_version:
      - 2
      - 0
    .max_flat_workgroup_size: 256
    .name:           _Z9k3_gatherPKfS0_PKdPKiS2_Pf
    .private_segment_fixed_size: 0
    .sgpr_count:     30
    .sgpr_spill_count: 0
    .symbol:         _Z9k3_gatherPKfS0_PKdPKiS2_Pf.kd
    .uniform_work_group_size: 1
    .uses_dynamic_stack: false
    .vgpr_count:     24
    .vgpr_spill_count: 0
    .wavefront_size: 64
